# attention K/V LDS-DMA addressed by scalar base + 32-bit lane offset (SALU pointer advance) instead of ten 64-bit VGPR adds per tile, on top of v24
# speedup vs baseline: 1.0212x; 1.0212x over previous
.LBB0_804:
	s_bfe_u32 s0, s66, 0x20001
	s_bfe_u32 s1, s78, 0x10007
	s_lshl_b32 s12, s1, 8
	s_lshl_b32 s44, s0, 9
	s_or_b32 s48, s44, s12
	s_mulk_i32 s0, 0x180
	s_mul_i32 s12, s1, 0xc0
	s_add_i32 s0, s0, s12
	s_lshl_b32 s50, s0, 1
	s_ashr_i32 s0, s78, 4
	s_lshl_b32 s12, s78, 1
	s_and_b32 s0, s0, -16
	s_and_b32 s44, s12, 8
	s_bfe_u32 s80, s78, 0x40003
	s_or_b32 s0, s0, s44
	s_xor_b32 s49, s80, 31
	s_ashr_i32 s0, s0, 3
	s_and_b32 s12, s12, 6
	s_lshl_b32 s83, s49, 8
	s_or_b32 s46, s12, s1
	s_ashr_i32 s1, s0, 31
	s_add_i32 s84, s83, s63
	s_lshr_b32 s81, s78, 3
	v_mov_b32_e32 v172, v1
	s_lshl_b64 s[52:53], s[0:1], 13
	s_ashr_i32 s12, s84, 31
	s_add_u32 s54, s52, s84
	v_and_b32_e32 v168, 31, v172
	v_or_b32_e32 v38, s54, v168
	s_addc_u32 s55, s53, s12
	v_mad_u64_u32 v[2:3], s[44:45], v38, s68, v[146:147]
	s_mul_i32 s82, s46, 0xc0
	v_bfe_u32 v173, v172, 5, 1
	v_mad_i32_i24 v3, s55, v162, v3
	s_lshl_b32 s12, s82, 1
	v_lshl_add_u64 v[2:3], v[2:3], 0, s[12:13]
	v_lshlrev_b32_e32 v148, 4, v173
	v_lshl_add_u64 v[40:41], v[2:3], 0, v[148:149]
	global_load_dwordx4 v[6:9], v[40:41], off
	global_load_dwordx4 v[14:17], v[40:41], off offset:32
	global_load_dwordx4 v[30:33], v[40:41], off offset:64
	global_load_dwordx4 v[34:37], v[40:41], off offset:96
	global_load_dwordx4 v[50:53], v[40:41], off offset:128
	global_load_dwordx4 v[26:29], v[40:41], off offset:160
	global_load_dwordx4 v[22:25], v[40:41], off offset:192
	global_load_dwordx4 v[18:21], v[40:41], off offset:224
	global_load_dwordx4 v[10:13], v[40:41], off offset:256
	global_load_dwordx4 v[42:45], v[40:41], off offset:288
	s_waitcnt lgkmcnt(0)
	global_load_dwordx4 v[2:5], v[40:41], off offset:320
	global_load_dwordx4 v[46:49], v[40:41], off offset:352
	v_and_b32_e32 v40, 32, v172
	v_mov_b32_e32 v39, s55
	s_mul_i32 s86, s0, 0x1800000
	s_mul_hi_i32 s51, s0, 0x1800000
	s_add_u32 s44, s33, s86
	s_addc_u32 s45, s58, s51
	s_lshl_b64 s[56:57], s[0:1], 24
	s_lshl_b32 s79, s46, 7
	s_add_u32 s44, s44, s12
	s_addc_u32 s45, s45, 0
	s_mov_b32 m0, s71
	s_add_u32 s0, s59, s56
	s_addc_u32 s1, s60, s57
	s_lshl_b32 s12, s46, 8
	s_add_u32 s46, s0, s12
	s_addc_u32 s47, s1, 0
	s_lshl_b32 s85, s49, 2
	s_add_i32 s85, s85, 4
	s_or_b32 s48, s56, s48
	s_add_u32 s48, s48, 0x29020000
	s_addc_u32 s49, s57, 0
	s_or_b32 s50, s86, s50
	s_add_u32 s50, s50, 0x23030000
	s_addc_u32 s51, s51, 0
	s_mov_b32 s12, 1
	s_movk_i32 s86, 0xff00
	s_waitcnt vmcnt(0)
	v_lshlrev_b32_e32 v227, 16, v26
	v_lshlrev_b32_e32 v177, 16, v6
	v_and_b32_e32 v174, 0xffff0000, v6
	v_lshlrev_b32_e32 v170, 16, v7
	v_and_b32_e32 v167, 0xffff0000, v7
	v_lshlrev_b32_e32 v180, 16, v8
	v_and_b32_e32 v176, 0xffff0000, v8
	v_lshlrev_b32_e32 v171, 16, v9
	v_and_b32_e32 v169, 0xffff0000, v9
	v_lshlrev_b32_e32 v185, 16, v14
	v_and_b32_e32 v182, 0xffff0000, v14
	v_lshlrev_b32_e32 v179, 16, v15
	v_and_b32_e32 v175, 0xffff0000, v15
	v_lshlrev_b32_e32 v187, 16, v16
	v_and_b32_e32 v183, 0xffff0000, v16
	v_lshlrev_b32_e32 v181, 16, v17
	v_and_b32_e32 v178, 0xffff0000, v17
	v_lshlrev_b32_e32 v201, 16, v34
	v_and_b32_e32 v198, 0xffff0000, v34
	v_lshlrev_b32_e32 v196, 16, v35
	v_and_b32_e32 v192, 0xffff0000, v35
	v_lshlrev_b32_e32 v202, 16, v36
	v_and_b32_e32 v199, 0xffff0000, v36
	v_lshlrev_b32_e32 v197, 16, v37
	v_and_b32_e32 v194, 0xffff0000, v37
	v_and_b32_e32 v228, 0xffff0000, v26
	global_load_dwordx4 v[142:145], v40, s[4:5] offset:704
	global_load_dwordx4 v[130:133], v40, s[4:5] offset:720
	global_load_dwordx4 v[6:9], v40, s[4:5] offset:592
	v_lshlrev_b32_e32 v229, 16, v27
	global_load_dwordx4 v[14:17], v40, s[4:5] offset:576
	v_and_b32_e32 v230, 0xffff0000, v27
	v_lshlrev_b32_e32 v231, 16, v28
	v_and_b32_e32 v232, 0xffff0000, v28
	v_lshlrev_b32_e32 v233, 16, v29
	v_and_b32_e32 v234, 0xffff0000, v29
	global_load_dwordx4 v[34:37], v40, s[4:5] offset:640
	global_load_dwordx4 v[156:159], v40, s[4:5] offset:656
	global_load_dwordx4 v[26:29], v40, s[4:5] offset:528
	v_mul_f32_e32 v209, v174, v174
	v_fmac_f32_e32 v209, v177, v177
	v_fmac_f32_e32 v209, v170, v170
	v_fmac_f32_e32 v209, v167, v167
	v_fmac_f32_e32 v209, v180, v180
	v_fmac_f32_e32 v209, v176, v176
	v_fmac_f32_e32 v209, v171, v171
	v_fmac_f32_e32 v209, v169, v169
	v_fmac_f32_e32 v209, v185, v185
	v_lshlrev_b32_e32 v193, 16, v30
	v_and_b32_e32 v190, 0xffff0000, v30
	v_lshlrev_b32_e32 v188, 16, v31
	v_and_b32_e32 v184, 0xffff0000, v31
	v_lshlrev_b32_e32 v195, 16, v32
	v_and_b32_e32 v191, 0xffff0000, v32
	v_lshlrev_b32_e32 v189, 16, v33
	v_and_b32_e32 v186, 0xffff0000, v33
	v_fmac_f32_e32 v209, v182, v182
	global_load_dwordx4 v[30:33], v40, s[4:5] offset:512
	v_fmac_f32_e32 v209, v179, v179
	v_fmac_f32_e32 v209, v175, v175
	v_fmac_f32_e32 v209, v187, v187
	v_fmac_f32_e32 v209, v183, v183
	v_fmac_f32_e32 v209, v181, v181
	v_fmac_f32_e32 v209, v178, v178
	v_fmac_f32_e32 v209, v193, v193
	v_fmac_f32_e32 v209, v190, v190
	v_fmac_f32_e32 v209, v188, v188
	v_fmac_f32_e32 v209, v184, v184
	v_fmac_f32_e32 v209, v195, v195
	v_fmac_f32_e32 v209, v191, v191
	v_fmac_f32_e32 v209, v189, v189
	v_fmac_f32_e32 v209, v186, v186
	v_fmac_f32_e32 v209, v201, v201
	v_fmac_f32_e32 v209, v198, v198
	v_fmac_f32_e32 v209, v196, v196
	v_fmac_f32_e32 v209, v192, v192
	v_fmac_f32_e32 v209, v202, v202
	v_fmac_f32_e32 v209, v199, v199
	v_fmac_f32_e32 v209, v197, v197
	v_lshlrev_b32_e32 v207, 16, v50
	v_fmac_f32_e32 v209, v194, v194
	v_and_b32_e32 v205, 0xffff0000, v50
	v_fmac_f32_e32 v209, v207, v207
	v_lshlrev_b32_e32 v203, 16, v51
	v_fmac_f32_e32 v209, v205, v205
	v_and_b32_e32 v200, 0xffff0000, v51
	v_fmac_f32_e32 v209, v203, v203
	v_lshlrev_b32_e32 v208, 16, v52
	v_fmac_f32_e32 v209, v200, v200
	v_and_b32_e32 v206, 0xffff0000, v52
	v_fmac_f32_e32 v209, v208, v208
	v_lshlrev_b32_e32 v204, 16, v53
	v_fmac_f32_e32 v209, v206, v206
	v_and_b32_e32 v226, 0xffff0000, v53
	v_fmac_f32_e32 v209, v204, v204
	v_fmac_f32_e32 v209, v226, v226
	v_fmac_f32_e32 v209, v227, v227
	v_fmac_f32_e32 v209, v228, v228
	v_fmac_f32_e32 v209, v229, v229
	v_fmac_f32_e32 v209, v230, v230
	global_load_dwordx4 v[110:113], v40, s[4:5] offset:16
	global_load_dwordx4 v[114:117], v40, s[4:5]
	global_load_dwordx4 v[102:105], v40, s[4:5] offset:80
	global_load_dwordx4 v[106:109], v40, s[4:5] offset:64
	global_load_dwordx4 v[94:97], v40, s[4:5] offset:144
	global_load_dwordx4 v[98:101], v40, s[4:5] offset:128
	global_load_dwordx4 v[86:89], v40, s[4:5] offset:208
	global_load_dwordx4 v[90:93], v40, s[4:5] offset:192
	global_load_dwordx4 v[78:81], v40, s[4:5] offset:272
	global_load_dwordx4 v[82:85], v40, s[4:5] offset:256
	global_load_dwordx4 v[70:73], v40, s[4:5] offset:336
	global_load_dwordx4 v[74:77], v40, s[4:5] offset:320
	global_load_dwordx4 v[62:65], v40, s[4:5] offset:400
	global_load_dwordx4 v[66:69], v40, s[4:5] offset:384
	global_load_dwordx4 v[54:57], v40, s[4:5] offset:464
	global_load_dwordx4 v[58:61], v40, s[4:5] offset:448
	v_fmac_f32_e32 v209, v231, v231
	v_fmac_f32_e32 v209, v232, v232
	v_fmac_f32_e32 v209, v233, v233
	v_fmac_f32_e32 v209, v234, v234
	s_waitcnt vmcnt(29)
	v_lshlrev_b32_e32 v235, 16, v22
	v_and_b32_e32 v236, 0xffff0000, v22
	v_fmac_f32_e32 v209, v235, v235
	v_lshlrev_b32_e32 v237, 16, v23
	v_fmac_f32_e32 v209, v236, v236
	v_and_b32_e32 v238, 0xffff0000, v23
	v_fmac_f32_e32 v209, v237, v237
	v_lshlrev_b32_e32 v239, 16, v24
	v_fmac_f32_e32 v209, v238, v238
	v_and_b32_e32 v240, 0xffff0000, v24
	v_fmac_f32_e32 v209, v239, v239
	v_lshlrev_b32_e32 v241, 16, v25
	v_fmac_f32_e32 v209, v240, v240
	v_and_b32_e32 v242, 0xffff0000, v25
	v_fmac_f32_e32 v209, v241, v241
	v_fmac_f32_e32 v209, v242, v242
	s_waitcnt vmcnt(28)
	v_lshlrev_b32_e32 v243, 16, v18
	v_and_b32_e32 v244, 0xffff0000, v18
	v_fmac_f32_e32 v209, v243, v243
	v_lshlrev_b32_e32 v245, 16, v19
	v_fmac_f32_e32 v209, v244, v244
	v_and_b32_e32 v246, 0xffff0000, v19
	v_fmac_f32_e32 v209, v245, v245
	v_lshlrev_b32_e32 v247, 16, v20
	v_fmac_f32_e32 v209, v246, v246
	v_and_b32_e32 v248, 0xffff0000, v20
	v_fmac_f32_e32 v209, v247, v247
	v_lshlrev_b32_e32 v249, 16, v21
	v_fmac_f32_e32 v209, v248, v248
	v_and_b32_e32 v250, 0xffff0000, v21
	v_fmac_f32_e32 v209, v249, v249
	s_waitcnt vmcnt(27)
	v_lshlrev_b32_e32 v223, 16, v10
	s_waitcnt vmcnt(25)
	v_lshlrev_b32_e32 v222, 16, v2
	v_fmac_f32_e32 v209, v250, v250
	s_waitcnt vmcnt(18)
	v_mov_b32_e32 v150, v158
	v_mov_b32_e32 v158, v156
	v_lshlrev_b32_e32 v156, 16, v3
	v_and_b32_e32 v160, 0xffff0000, v3
	v_and_b32_e32 v225, 0xffff0000, v10
	v_and_b32_e32 v224, 0xffff0000, v2
	v_pk_mul_f32 v[2:3], v[222:223], v[222:223]
	v_mov_b32_e32 v134, v144
	v_mov_b32_e32 v140, v142
	v_lshlrev_b32_e32 v142, 16, v5
	s_waitcnt vmcnt(17)
	v_mov_b32_e32 v151, v28
	v_and_b32_e32 v144, 0xffff0000, v5
	v_mov_b32_e32 v28, v159
	v_lshlrev_b32_e32 v152, 16, v4
	v_mov_b32_e32 v159, v26
	v_and_b32_e32 v154, 0xffff0000, v4
	v_mov_b32_e32 v26, v157
	v_lshlrev_b32_e32 v157, 16, v11
	v_add_f32_e32 v3, v3, v209
	v_pk_mul_f32 v[4:5], v[224:225], v[224:225]
	v_lshlrev_b32_e32 v119, 16, v45
	v_and_b32_e32 v121, 0xffff0000, v45
	v_lshlrev_b32_e32 v125, 16, v44
	v_and_b32_e32 v127, 0xffff0000, v44
	v_pk_mul_f32 v[44:45], v[156:157], v[156:157]
	v_and_b32_e32 v161, 0xffff0000, v11
	v_add_f32_e32 v3, v5, v3
	v_mov_b32_e32 v122, v132
	v_mov_b32_e32 v128, v130
	v_lshlrev_b32_e32 v130, 16, v47
	v_and_b32_e32 v132, 0xffff0000, v47
	v_lshlrev_b32_e32 v136, 16, v46
	v_and_b32_e32 v138, 0xffff0000, v46
	v_lshlrev_b32_e32 v153, 16, v12
	v_pk_mul_f32 v[46:47], v[160:161], v[160:161]
	v_add_f32_e32 v3, v45, v3
	v_mov_b32_e32 v123, v8
	v_mov_b32_e32 v8, v133
	v_mov_b32_e32 v129, v6
	v_mov_b32_e32 v6, v131
	v_lshlrev_b32_e32 v131, 16, v43
	v_and_b32_e32 v133, 0xffff0000, v43
	v_lshlrev_b32_e32 v137, 16, v42
	v_and_b32_e32 v139, 0xffff0000, v42
	v_pk_mul_f32 v[42:43], v[152:153], v[152:153]
	v_and_b32_e32 v155, 0xffff0000, v12
	v_add_f32_e32 v3, v47, v3
	v_mov_b32_e32 v141, v14
	v_mov_b32_e32 v14, v143
	v_lshlrev_b32_e32 v143, 16, v13
	v_pk_mul_f32 v[220:221], v[154:155], v[154:155]
	v_add_f32_e32 v3, v43, v3
	v_mov_b32_e32 v135, v16
	v_mov_b32_e32 v16, v145
	v_pk_mul_f32 v[216:217], v[142:143], v[142:143]
	v_and_b32_e32 v145, 0xffff0000, v13
	v_add_f32_e32 v3, v221, v3
	v_pk_mul_f32 v[218:219], v[144:145], v[144:145]
	v_add_f32_e32 v3, v217, v3
	v_pk_mul_f32 v[212:213], v[136:137], v[136:137]
	v_add_f32_e32 v3, v219, v3
	v_pk_mul_f32 v[214:215], v[138:139], v[138:139]
	v_add_f32_e32 v3, v213, v3
	v_add_f32_e32 v3, v215, v3
	v_fmac_f32_e32 v3, v131, v131
	v_fmac_f32_e32 v3, v133, v133
	v_fmac_f32_e32 v3, v125, v125
	v_fmac_f32_e32 v3, v127, v127
	v_fmac_f32_e32 v3, v119, v119
	v_fmac_f32_e32 v3, v121, v121
	v_add_f32_e32 v2, v2, v3
	v_add_f32_e32 v43, v4, v2
	v_add_f32_e32 v43, v44, v43
	v_add_f32_e32 v43, v46, v43
	v_add_f32_e32 v209, v42, v43
	v_add_f32_e32 v209, v220, v209
	v_add_f32_e32 v209, v216, v209
	v_add_f32_e32 v209, v218, v209
	v_mov_b32_e32 v218, v132
	v_mov_b32_e32 v219, v130
	v_add_f32_e32 v209, v212, v209
	v_lshlrev_b64 v[18:19], 8, v[38:39]
	v_lshlrev_b32_e32 v124, 16, v48
	v_and_b32_e32 v126, 0xffff0000, v48
	v_pk_mul_f32 v[218:219], v[218:219], v[218:219]
	s_waitcnt vmcnt(16)
	v_mov_b32_e32 v213, v32
	v_add_f32_e32 v32, v214, v209
	v_lshl_add_u64 v[18:19], s[10:11], 0, v[18:19]
	v_lshlrev_b32_e32 v20, 6, v173
	v_mov_b32_e32 v21, v149
	v_mov_b32_e32 v216, v126
	v_mov_b32_e32 v217, v124
	v_add_f32_e32 v32, v219, v32
	v_lshl_add_u64 v[210:211], v[18:19], 0, v[20:21]
	v_lshlrev_b32_e32 v118, 16, v49
	v_and_b32_e32 v120, 0xffff0000, v49
	v_pk_mul_f32 v[216:217], v[216:217], v[216:217]
	v_add_f32_e32 v32, v218, v32
	global_load_dwordx4 v[18:21], v[210:211], off offset:48
	global_load_dwordx4 v[22:25], v[210:211], off offset:32
	global_load_dwordx4 v[38:41], v[210:211], off offset:16
	global_load_dwordx4 v[50:53], v[210:211], off
	global_load_dwordx4 v[2:5], v[210:211], off offset:176
	global_load_dwordx4 v[10:13], v[210:211], off offset:160
	global_load_dwordx4 v[42:45], v[210:211], off offset:144
	global_load_dwordx4 v[46:49], v[210:211], off offset:128
	v_mov_b32_e32 v210, v120
	v_mov_b32_e32 v211, v118
	v_add_f32_e32 v32, v217, v32
	v_pk_mul_f32 v[210:211], v[210:211], v[210:211]
	v_add_f32_e32 v32, v216, v32
	v_add_f32_e32 v32, v211, v32
	v_add_f32_e32 v32, v210, v32
	v_mov_b32_e32 v212, v36
	v_mov_b32_e32 v36, v32
	s_nop 1
	v_permlane32_swap_b32_e32 v32, v36
	v_add_f32_e32 v32, v32, v36
	v_fmamk_f32 v32, v32, 0x3baaaaab, v163
	v_mul_f32_e32 v36, 0x4b800000, v32
	v_cmp_gt_f32_e32 vcc, s69, v32
	s_nop 1
	v_cndmask_b32_e32 v32, v32, v36, vcc
	v_rsq_f32_e32 v209, v32
	v_mov_b32_e32 v32, v37
	v_mov_b32_e32 v37, v30
	v_mov_b32_e32 v36, v34
	v_mul_f32_e32 v30, 0x45800000, v209
	v_cndmask_b32_e32 v30, v209, v30, vcc
	v_mul_f32_e32 v34, 0x3dd53b94, v30
	s_waitcnt vmcnt(22)
	v_mul_f32_e32 v30, v114, v34
	v_mul_f32_e32 v114, v30, v177
	v_mul_f32_e32 v30, v110, v34
	v_mul_f32_e32 v110, v30, v180
	v_mul_f32_e32 v30, v115, v34
	v_mul_f32_e32 v115, v30, v174
	v_mul_f32_e32 v30, v111, v34
	v_mul_f32_e32 v111, v30, v176
	v_mul_f32_e32 v30, v116, v34
	v_mul_f32_e32 v116, v30, v170
	v_mul_f32_e32 v30, v112, v34
	v_mul_f32_e32 v112, v30, v171
	v_mul_f32_e32 v30, v117, v34
	v_mul_f32_e32 v117, v30, v167
	v_mul_f32_e32 v30, v113, v34
	v_mul_f32_e32 v113, v30, v169
	s_waitcnt vmcnt(20)
	v_mul_f32_e32 v30, v106, v34
	v_mul_f32_e32 v106, v30, v185
	v_mul_f32_e32 v30, v102, v34
	v_mul_f32_e32 v167, v30, v187
	v_mul_f32_e32 v30, v107, v34
	v_mul_f32_e32 v102, v30, v182
	v_mul_f32_e32 v30, v103, v34
	v_mul_f32_e32 v107, v30, v183
	v_mul_f32_e32 v30, v108, v34
	v_mul_f32_e32 v103, v30, v179
	v_mul_f32_e32 v30, v104, v34
	v_mul_f32_e32 v108, v30, v181
	v_mul_f32_e32 v30, v109, v34
	v_mul_f32_e32 v104, v30, v175
	v_mul_f32_e32 v30, v105, v34
	v_mul_f32_e32 v105, v30, v178
	s_waitcnt vmcnt(18)
	v_mul_f32_e32 v30, v98, v34
	v_mul_f32_e32 v109, v30, v193
	v_mul_f32_e32 v30, v94, v34
	v_mul_f32_e32 v94, v30, v195
	v_mul_f32_e32 v30, v99, v34
	v_mul_f32_e32 v169, v30, v190
	v_mul_f32_e32 v30, v95, v34
	v_mul_f32_e32 v95, v30, v191
	v_mul_f32_e32 v30, v100, v34
	v_mul_f32_e32 v170, v30, v188
	v_mul_f32_e32 v30, v96, v34
	v_mul_f32_e32 v96, v30, v189
	v_mul_f32_e32 v30, v101, v34
	v_mul_f32_e32 v171, v30, v184
	v_mul_f32_e32 v30, v97, v34
	v_mul_f32_e32 v97, v30, v186
	s_waitcnt vmcnt(16)
	v_mul_f32_e32 v30, v90, v34
	v_mul_f32_e32 v90, v30, v201
	v_mul_f32_e32 v30, v86, v34
	v_mul_f32_e32 v86, v30, v202
	v_mul_f32_e32 v30, v91, v34
	v_mul_f32_e32 v91, v30, v198
	v_mul_f32_e32 v30, v87, v34
	v_mul_f32_e32 v87, v30, v199
	v_mul_f32_e32 v30, v92, v34
	v_mul_f32_e32 v92, v30, v196
	v_mul_f32_e32 v30, v88, v34
	v_mul_f32_e32 v88, v30, v197
	v_mul_f32_e32 v30, v93, v34
	v_mul_f32_e32 v93, v30, v192
	v_mul_f32_e32 v30, v89, v34
	v_mul_f32_e32 v89, v30, v194
	s_waitcnt vmcnt(14)
	v_mul_f32_e32 v30, v82, v34
	v_mul_f32_e32 v82, v30, v207
	v_mul_f32_e32 v30, v34, v78
	v_mul_f32_e32 v78, v30, v208
	v_mul_f32_e32 v30, v83, v34
	v_mul_f32_e32 v83, v30, v205
	v_mul_f32_e32 v30, v34, v79
	v_mul_f32_e32 v79, v30, v206
	v_mul_f32_e32 v30, v84, v34
	v_mul_f32_e32 v84, v30, v203
	v_mul_f32_e32 v30, v34, v80
	v_mul_f32_e32 v80, v30, v204
	v_mul_f32_e32 v30, v85, v34
	v_mul_f32_e32 v85, v30, v200
	v_mul_f32_e32 v30, v34, v81
	v_mul_f32_e32 v81, v30, v226
	s_waitcnt vmcnt(12)
	v_mul_f32_e32 v30, v34, v74
	v_mul_f32_e32 v74, v30, v227
	v_mul_f32_e32 v30, v34, v70
	v_mul_f32_e32 v70, v30, v231
	v_mul_f32_e32 v30, v34, v75
	v_mul_f32_e32 v75, v30, v228
	v_mul_f32_e32 v30, v34, v71
	v_mul_f32_e32 v71, v30, v232
	v_mul_f32_e32 v30, v34, v76
	v_mul_f32_e32 v76, v30, v229
	v_mul_f32_e32 v30, v34, v72
	v_mul_f32_e32 v72, v30, v233
	v_mul_f32_e32 v30, v34, v77
	v_mul_f32_e32 v77, v30, v230
	v_mul_f32_e32 v30, v34, v73
	v_mul_f32_e32 v73, v30, v234
	s_waitcnt vmcnt(10)
	v_mul_f32_e32 v30, v34, v66
	v_mul_f32_e32 v174, v30, v235
	v_mul_f32_e32 v30, v34, v62
	v_mul_f32_e32 v175, v30, v239
	v_mul_f32_e32 v30, v34, v67
	v_mul_f32_e32 v176, v30, v236
	v_mul_f32_e32 v30, v34, v63
	v_mul_f32_e32 v177, v30, v240
	v_mul_f32_e32 v30, v34, v68
	v_mul_f32_e32 v68, v30, v237
	v_mul_f32_e32 v30, v34, v64
	v_mul_f32_e32 v178, v30, v241
	v_mul_f32_e32 v30, v34, v69
	v_mul_f32_e32 v69, v30, v238
	v_mul_f32_e32 v30, v34, v65
	v_mul_f32_e32 v179, v30, v242
	s_waitcnt vmcnt(8)
	v_mul_f32_e32 v30, v34, v58
	v_mul_f32_e32 v180, v30, v243
	v_mul_f32_e32 v30, v34, v54
	v_mul_f32_e32 v181, v30, v247
	v_mul_f32_e32 v30, v34, v59
	v_mul_f32_e32 v182, v30, v244
	v_mul_f32_e32 v30, v34, v55
	v_mul_f32_e32 v183, v30, v248
	v_mul_f32_e32 v30, v34, v60
	v_mul_f32_e32 v184, v30, v245
	v_mul_f32_e32 v30, v34, v56
	v_mul_f32_e32 v185, v30, v249
	v_mul_f32_e32 v30, v34, v61
	v_mul_f32_e32 v186, v30, v246
	v_mul_f32_e32 v30, v34, v57
	v_pk_mul_f32 v[36:37], v[34:35], v[36:37] op_sel_hi:[0,1]
	v_mul_f32_e32 v187, v30, v250
	v_pk_mul_f32 v[36:37], v[36:37], v[222:223]
	v_mov_b32_e32 v30, v35
	v_pk_mul_f32 v[54:55], v[34:35], v[158:159] op_sel_hi:[0,1]
	v_pk_mul_f32 v[30:31], v[34:35], v[30:31] op_sel_hi:[0,1]
	v_pk_mul_f32 v[26:27], v[34:35], v[26:27] op_sel_hi:[0,1]
	v_pk_mul_f32 v[56:57], v[34:35], v[212:213] op_sel_hi:[0,1]
	v_pk_mul_f32 v[58:59], v[34:35], v[150:151] op_sel_hi:[0,1]
	v_pk_mul_f32 v[32:33], v[34:35], v[32:33] op_sel_hi:[0,1]
	v_pk_mul_f32 v[28:29], v[34:35], v[28:29] op_sel_hi:[0,1]
	v_pk_mul_f32 v[60:61], v[34:35], v[140:141] op_sel_hi:[0,1]
	v_pk_mul_f32 v[62:63], v[34:35], v[128:129] op_sel_hi:[0,1]
	v_pk_mul_f32 v[14:15], v[34:35], v[14:15] op_sel_hi:[0,1]
	v_pk_mul_f32 v[6:7], v[34:35], v[6:7] op_sel_hi:[0,1]
	v_pk_mul_f32 v[64:65], v[34:35], v[134:135] op_sel_hi:[0,1]
	v_pk_mul_f32 v[66:67], v[34:35], v[122:123] op_sel_hi:[0,1]
	v_pk_mul_f32 v[16:17], v[34:35], v[16:17] op_sel_hi:[0,1]
	v_pk_mul_f32 v[8:9], v[34:35], v[8:9] op_sel_hi:[0,1]
	s_waitcnt vmcnt(4)
	v_pk_mul_f32 v[34:35], v[36:37], v[50:51] op_sel:[1,0] op_sel_hi:[0,1]
	v_pk_mul_f32 v[30:31], v[30:31], v[224:225]
	v_pk_mul_f32 v[64:65], v[64:65], v[130:131]
	v_sub_f32_e32 v130, v34, v35
	v_pk_mul_f32 v[34:35], v[36:37], v[50:51]
	v_pk_mul_f32 v[56:57], v[56:57], v[156:157]
	v_add_f32_e32 v36, v35, v34
	v_pk_mul_f32 v[34:35], v[30:31], v[52:53] op_sel:[1,0] op_sel_hi:[0,1]
	v_pk_mul_f32 v[30:31], v[30:31], v[52:53]
	v_sub_f32_e32 v34, v34, v35
	v_add_f32_e32 v35, v31, v30
	v_pk_mul_f32 v[30:31], v[56:57], v[38:39] op_sel:[1,0] op_sel_hi:[0,1]
	v_pk_mul_f32 v[32:33], v[32:33], v[160:161]
	v_sub_f32_e32 v37, v30, v31
	v_pk_mul_f32 v[30:31], v[56:57], v[38:39]
	v_pk_mul_f32 v[54:55], v[54:55], v[152:153]
	v_add_f32_e32 v38, v31, v30
	v_pk_mul_f32 v[30:31], v[32:33], v[40:41] op_sel:[1,0] op_sel_hi:[0,1]
	v_sub_f32_e32 v39, v30, v31
	v_pk_mul_f32 v[30:31], v[32:33], v[40:41]
	v_pk_mul_f32 v[26:27], v[26:27], v[154:155]
	v_add_f32_e32 v32, v31, v30
	v_pk_mul_f32 v[30:31], v[54:55], v[22:23] op_sel:[1,0] op_sel_hi:[0,1]
	v_pk_mul_f32 v[22:23], v[54:55], v[22:23]
	v_sub_f32_e32 v30, v30, v31
	v_add_f32_e32 v31, v23, v22
	v_pk_mul_f32 v[22:23], v[26:27], v[24:25] op_sel:[1,0] op_sel_hi:[0,1]
	v_pk_mul_f32 v[58:59], v[58:59], v[142:143]
	v_sub_f32_e32 v33, v22, v23
	v_pk_mul_f32 v[22:23], v[26:27], v[24:25]
	v_pk_mul_f32 v[28:29], v[28:29], v[144:145]
	v_add_f32_e32 v24, v23, v22
	v_pk_mul_f32 v[22:23], v[58:59], v[18:19] op_sel:[1,0] op_sel_hi:[0,1]
	v_pk_mul_f32 v[18:19], v[58:59], v[18:19]
	v_sub_f32_e32 v22, v22, v23
	v_add_f32_e32 v23, v19, v18
	v_pk_mul_f32 v[18:19], v[28:29], v[20:21] op_sel:[1,0] op_sel_hi:[0,1]
	v_pk_mul_f32 v[60:61], v[60:61], v[136:137]
	v_sub_f32_e32 v25, v18, v19
	v_pk_mul_f32 v[18:19], v[28:29], v[20:21]
	v_pk_mul_f32 v[14:15], v[14:15], v[138:139]
	v_add_f32_e32 v20, v19, v18
	s_waitcnt vmcnt(0)
	v_pk_mul_f32 v[18:19], v[60:61], v[46:47] op_sel:[1,0] op_sel_hi:[0,1]
	v_sub_f32_e32 v21, v18, v19
	v_pk_mul_f32 v[18:19], v[60:61], v[46:47]
	v_pk_mul_f32 v[16:17], v[16:17], v[132:133]
	v_add_f32_e32 v26, v19, v18
	v_pk_mul_f32 v[18:19], v[14:15], v[48:49] op_sel:[1,0] op_sel_hi:[0,1]
	v_pk_mul_f32 v[14:15], v[14:15], v[48:49]
	v_sub_f32_e32 v18, v18, v19
	v_add_f32_e32 v19, v15, v14
	v_pk_mul_f32 v[14:15], v[64:65], v[42:43] op_sel:[1,0] op_sel_hi:[0,1]
	v_sub_f32_e32 v27, v14, v15
	v_pk_mul_f32 v[14:15], v[64:65], v[42:43]
	v_pk_mul_f32 v[62:63], v[62:63], v[124:125]
	v_add_f32_e32 v28, v15, v14
	v_pk_mul_f32 v[14:15], v[16:17], v[44:45] op_sel:[1,0] op_sel_hi:[0,1]
	v_sub_f32_e32 v29, v14, v15
	v_pk_mul_f32 v[14:15], v[16:17], v[44:45]
	v_pk_mul_f32 v[6:7], v[6:7], v[126:127]
	v_add_f32_e32 v16, v15, v14
	v_pk_mul_f32 v[14:15], v[62:63], v[10:11] op_sel:[1,0] op_sel_hi:[0,1]
	v_pk_mul_f32 v[10:11], v[62:63], v[10:11]
	v_pk_mul_f32 v[66:67], v[66:67], v[118:119]
	v_sub_f32_e32 v14, v14, v15
	v_add_f32_e32 v15, v11, v10
	v_pk_mul_f32 v[10:11], v[6:7], v[12:13] op_sel:[1,0] op_sel_hi:[0,1]
	v_pk_mul_f32 v[6:7], v[6:7], v[12:13]
	v_pk_mul_f32 v[8:9], v[8:9], v[120:121]
	v_sub_f32_e32 v10, v10, v11
	v_add_f32_e32 v11, v7, v6
	v_pk_mul_f32 v[6:7], v[66:67], v[2:3] op_sel:[1,0] op_sel_hi:[0,1]
	v_pk_mul_f32 v[2:3], v[66:67], v[2:3]
	v_sub_f32_e32 v6, v6, v7
	v_add_f32_e32 v7, v3, v2
	v_pk_mul_f32 v[2:3], v[8:9], v[4:5] op_sel:[1,0] op_sel_hi:[0,1]
	v_sub_f32_e32 v12, v2, v3
	v_pk_mul_f32 v[2:3], v[8:9], v[4:5]
	v_cvt_pk_bf16_f32 v98, v114, v115
	v_cvt_pk_bf16_f32 v99, v116, v117
	v_cvt_pk_bf16_f32 v100, v110, v111
	v_cvt_pk_bf16_f32 v101, v112, v113
	v_cvt_pk_bf16_f32 v102, v106, v102
	s_nop 0
	v_add_f32_e32 v2, v3, v2
	v_cvt_pk_bf16_f32 v103, v103, v104
	v_cvt_pk_bf16_f32 v104, v167, v107
	v_cvt_pk_bf16_f32 v105, v108, v105
	v_cvt_pk_bf16_f32 v106, v109, v169
	v_cvt_pk_bf16_f32 v107, v170, v171
	v_cvt_pk_bf16_f32 v108, v94, v95
	v_cvt_pk_bf16_f32 v109, v96, v97
	v_cvt_pk_bf16_f32 v110, v90, v91
	v_cvt_pk_bf16_f32 v111, v92, v93
	v_cvt_pk_bf16_f32 v112, v86, v87
	v_cvt_pk_bf16_f32 v113, v88, v89
	v_cvt_pk_bf16_f32 v114, v82, v83
	v_cvt_pk_bf16_f32 v115, v84, v85
	v_cvt_pk_bf16_f32 v116, v78, v79
	v_cvt_pk_bf16_f32 v117, v80, v81
	v_cvt_pk_bf16_f32 v118, v74, v75
	v_cvt_pk_bf16_f32 v119, v76, v77
	v_cvt_pk_bf16_f32 v120, v70, v71
	v_cvt_pk_bf16_f32 v121, v72, v73
	v_cvt_pk_bf16_f32 v122, v174, v176
	v_cvt_pk_bf16_f32 v123, v68, v69
	v_cvt_pk_bf16_f32 v124, v175, v177
	v_cvt_pk_bf16_f32 v125, v178, v179
	v_cvt_pk_bf16_f32 v126, v180, v182
	v_cvt_pk_bf16_f32 v127, v184, v186
	v_cvt_pk_bf16_f32 v128, v181, v183
	v_cvt_pk_bf16_f32 v129, v185, v187
	v_cvt_pk_bf16_f32 v130, v130, v34
	v_cvt_pk_bf16_f32 v131, v37, v39
	v_cvt_pk_bf16_f32 v132, v30, v33
	v_cvt_pk_bf16_f32 v133, v22, v25
	v_cvt_pk_bf16_f32 v134, v21, v18
	v_cvt_pk_bf16_f32 v135, v27, v29
	v_cvt_pk_bf16_f32 v136, v14, v10
	v_cvt_pk_bf16_f32 v137, v6, v12
	v_cvt_pk_bf16_f32 v138, v36, v35
	v_cvt_pk_bf16_f32 v139, v38, v32
	v_cvt_pk_bf16_f32 v140, v31, v24
	v_cvt_pk_bf16_f32 v141, v23, v20
	v_cvt_pk_bf16_f32 v142, v26, v19
	v_cvt_pk_bf16_f32 v143, v28, v16
	v_cvt_pk_bf16_f32 v144, v15, v11
	v_cvt_pk_bf16_f32 v145, v7, v2
	v_mul_hi_i32 v2, v172, s70
	v_lshrrev_b32_e32 v3, 31, v2
	v_ashrrev_i32_e32 v2, 2, v2
	v_add_u32_e32 v2, v2, v3
	v_mul_lo_u32 v3, v2, 24
	v_sub_u32_e32 v3, v172, v3
	v_lshrrev_b32_e32 v16, 1, v2
	v_bitop3_b32 v3, v16, v3, 7 bitop3:0x6c
	v_mul_lo_u32 v2, v2, s68
	v_lshl_add_u32 v2, v3, 4, v2
	v_add_u32_e32 v3, 0x200, v172
	v_mul_hi_i32 v4, v3, s70
	v_lshrrev_b32_e32 v5, 31, v4
	v_ashrrev_i32_e32 v4, 2, v4
	v_add_u32_e32 v4, v4, v5
	v_mul_lo_u32 v5, v4, 24
	v_sub_u32_e32 v5, v3, v5
	v_lshrrev_b32_e32 v16, 1, v4
	v_bitop3_b32 v5, v16, v5, 7 bitop3:0x6c
	v_mul_lo_u32 v4, v4, s68
	v_lshl_add_u32 v4, v5, 4, v4
	v_add_u32_e32 v5, 0x400, v172
	v_mul_hi_i32 v6, v5, s70
	v_lshrrev_b32_e32 v7, 31, v6
	v_ashrrev_i32_e32 v6, 2, v6
	v_add_u32_e32 v6, v6, v7
	v_mul_lo_u32 v7, v6, 24
	v_sub_u32_e32 v5, v5, v7
	v_lshrrev_b32_e32 v16, 1, v6
	v_bitop3_b32 v5, v16, v5, 7 bitop3:0x6c
	v_mul_lo_u32 v6, v6, s68
	v_ashrrev_i32_e32 v9, 4, v172
	v_lshl_add_u32 v6, v5, 4, v6
	v_bfe_u32 v5, v172, 2, 2
	v_lshrrev_b32_e32 v7, 1, v172
	v_and_b32_e32 v10, 0x1ffff0, v9
	v_lshrrev_b32_e32 v9, 1, v9
	v_ashrrev_i32_e32 v3, 4, v3
	v_and_or_b32 v5, v7, 8, v5
	v_and_b32_e32 v7, 0x60, v172
	v_lshlrev_b32_e32 v8, 3, v172
	v_and_b32_e32 v9, 4, v9
	v_and_b32_e32 v11, 0x1ffff0, v3
	v_lshrrev_b32_e32 v3, 1, v3
	v_and_or_b32 v7, v8, 24, v7
	v_or3_b32 v9, v10, v9, v5
	v_and_b32_e32 v3, 4, v3
	s_barrier
	global_load_lds_dwordx4 v2, s[44:45]
	s_mov_b32 m0, s72
	v_lshlrev_b32_e32 v7, 1, v7
	v_lshlrev_b32_e32 v10, 11, v9
	v_or3_b32 v3, v11, v3, v5
	global_load_lds_dwordx4 v4, s[44:45]
	s_mov_b32 m0, s73
	v_or_b32_e32 v9, v10, v7
	v_lshlrev_b32_e32 v11, 11, v3
	global_load_lds_dwordx4 v6, s[44:45]
	s_mov_b32 m0, s64
	v_or_b32_e32 v3, v11, v7
	global_load_lds_dwordx4 v9, s[46:47]
	s_mov_b32 m0, s74
	v_lshlrev_b32_e32 v13, 1, v172
	global_load_lds_dwordx4 v3, s[46:47]
	v_lshlrev_b32_e32 v9, 4, v172
	v_and_b32_e32 v14, 32, v13
	v_or_b32_e32 v3, 32, v148
	v_mul_u32_u24_e32 v5, 0x180, v168
	v_and_b32_e32 v7, 0x70, v8
	v_and_b32_e32 v12, 0xc0, v9
	v_and_or_b32 v8, v8, s75, v14
	v_and_b32_e32 v167, 63, v172
	v_bitop3_b32 v169, v3, v5, v7 bitop3:0xde
	v_or_b32_e32 v3, 64, v148
	v_add3_u32 v172, v12, 0, v8
	v_and_b32_e32 v12, 0xc0, v13
	v_and_b32_e32 v13, 48, v9
	v_bitop3_b32 v170, v3, v5, v7 bitop3:0xde
	v_or_b32_e32 v3, 0x60, v148
	v_or3_b32 v8, v11, v12, v13
	v_mov_b32_e32 v9, v149
	v_bitop3_b32 v161, v148, v5, v7 bitop3:0xde
	v_bitop3_b32 v171, v3, v5, v7 bitop3:0xde
	v_mov_b32_e32 v3, v149
	v_mov_b32_e32 v5, v149
	v_mov_b32_e32 v7, v149
	v_mul_i32_i24_e32 v15, -4, v173
	v_lshl_add_u64 v[150:151], s[48:49], 0, v[8:9]
	v_mov_b32_e32 v240, v8
	v_or3_b32 v8, v10, v12, v13
	v_mov_b32_e32 v16, v149
	v_mov_b32_e32 v17, v149
	v_lshl_add_u32 v160, v168, 2, s65
	v_lshl_add_u64 v[152:153], s[48:49], 0, v[8:9]
	v_mov_b32_e32 v241, v8
	v_lshl_add_u64 v[154:155], s[50:51], 0, v[6:7]
	v_mov_b32_e32 v242, v6
	v_lshl_add_u64 v[156:157], s[50:51], 0, v[4:5]
	v_mov_b32_e32 v243, v4
	v_lshl_add_u64 v[158:159], s[50:51], 0, v[2:3]
	v_mov_b32_e32 v244, v2
	s_add_u32 s94, s2, s50
	s_addc_u32 s95, s3, s51
	s_add_u32 s96, s2, s48
	s_addc_u32 s97, s3, s49
	v_add3_u32 v168, s63, v15, v168
	v_mov_b32_e32 v2, v149
	v_mov_b32_e32 v4, v149
	v_mov_b32_e32 v6, v149
	v_mov_b32_e32 v8, v149
	v_mov_b32_e32 v10, v149
	v_mov_b32_e32 v11, v149
	v_mov_b32_e32 v12, v149
	v_mov_b32_e32 v13, v149
	v_mov_b32_e32 v14, v149
	v_mov_b32_e32 v15, v149
	v_mov_b64_e32 v[32:33], v[16:17]
	v_mov_b64_e32 v[48:49], v[16:17]
	v_mov_b64_e32 v[64:65], v[16:17]
	v_cmp_gt_u32_e64 s[0:1], 32, v167
	v_mov_b32_e32 v173, 0
	v_mov_b32_e32 v206, 0
	v_mov_b32_e32 v207, 0
	v_mov_b32_e32 v208, 0
	v_mov_b32_e32 v209, 0
	v_mov_b32_e32 v210, 0
	v_mov_b32_e32 v211, 0
	v_mov_b32_e32 v212, 0
	v_mov_b32_e32 v213, 0
	v_mov_b32_e32 v214, 0
	v_mov_b32_e32 v215, 0
	v_mov_b32_e32 v216, 0
	v_mov_b32_e32 v217, 0
	v_mov_b32_e32 v218, 0
	v_mov_b32_e32 v219, 0
	v_mov_b32_e32 v220, 0
	v_mov_b32_e32 v221, 0
	v_mov_b64_e32 v[30:31], v[14:15]
	v_mov_b64_e32 v[28:29], v[12:13]
	v_mov_b64_e32 v[26:27], v[10:11]
	v_mov_b64_e32 v[24:25], v[8:9]
	v_mov_b64_e32 v[22:23], v[6:7]
	v_mov_b64_e32 v[20:21], v[4:5]
	v_mov_b64_e32 v[18:19], v[2:3]
	v_mov_b64_e32 v[46:47], v[14:15]
	v_mov_b64_e32 v[44:45], v[12:13]
	v_mov_b64_e32 v[42:43], v[10:11]
	v_mov_b64_e32 v[40:41], v[8:9]
	v_mov_b64_e32 v[38:39], v[6:7]
	v_mov_b64_e32 v[36:37], v[4:5]
	v_mov_b64_e32 v[34:35], v[2:3]
	v_mov_b64_e32 v[62:63], v[14:15]
	v_mov_b64_e32 v[60:61], v[12:13]
	v_mov_b64_e32 v[58:59], v[10:11]
	v_mov_b64_e32 v[56:57], v[8:9]
	v_mov_b64_e32 v[54:55], v[6:7]
	v_mov_b64_e32 v[52:53], v[4:5]
	v_mov_b64_e32 v[50:51], v[2:3]
	v_mov_b32_e32 v174, 0
.LBB0_805:
	s_add_i32 s56, s12, -1
	s_waitcnt vmcnt(0)
	s_and_b32 s87, s56, 1
	s_cmp_ge_u32 s12, s85
	s_waitcnt vmcnt(0) lgkmcnt(0)
	s_barrier
	s_cbranch_scc1 .LBB0_807
	s_xor_b32 s56, s87, 1
	s_mulk_i32 s56, 0x6000
	s_add_i32 s56, s64, s56
	s_add_i32 m0, s56, 0x8000
	s_nop 0
	global_load_lds_dwordx4 v244, s[94:95]
	s_add_i32 m0, s56, 0xa000
	s_nop 0
	global_load_lds_dwordx4 v243, s[94:95]
	s_add_i32 m0, s56, 0xc000
	s_lshl_b32 s56, s87, 14
	s_xor_b32 s56, s56, 0x4000
	s_add_i32 s56, s64, s56
	global_load_lds_dwordx4 v242, s[94:95]
	s_mov_b32 m0, s56
	s_nop 0
	global_load_lds_dwordx4 v241, s[96:97]
	s_add_i32 m0, s56, 0x2000
	s_nop 0
	global_load_lds_dwordx4 v240, s[96:97]



.LBB0_813:
	v_cvt_pk_bf16_f32 v178, v82, v175
	v_cvt_pk_bf16_f32 v179, v84, v85
	v_cvt_pk_bf16_f32 v180, v86, v87
	v_cvt_pk_bf16_f32 v181, v88, v176
	v_cvt_pk_bf16_f32 v84, v89, v90
	v_cvt_pk_bf16_f32 v85, v91, v92
	v_cvt_pk_bf16_f32 v86, v93, v94
	v_cvt_pk_bf16_f32 v87, v95, v96
	v_cvt_pk_bf16_f32 v66, v66, v67
	v_cvt_pk_bf16_f32 v67, v68, v69
	v_cvt_pk_bf16_f32 v68, v70, v71
	v_cvt_pk_bf16_f32 v69, v72, v83
	v_cvt_pk_bf16_f32 v70, v73, v74
	v_cvt_pk_bf16_f32 v71, v75, v76
	v_cvt_pk_bf16_f32 v72, v77, v78
	v_cvt_pk_bf16_f32 v73, v80, v81
	v_lshl_add_u32 v78, s87, 14, v172
	ds_read_b64_tr_b16 v[74:75], v78 offset:0
	ds_read_b64_tr_b16 v[76:77], v78 offset:0x800
	ds_read_b64_tr_b16 v[80:81], v78 offset:0x1000
	ds_read_b64_tr_b16 v[82:83], v78 offset:0x1800
	ds_read_b64_tr_b16 v[88:89], v78 offset:0x2000
	ds_read_b64_tr_b16 v[90:91], v78 offset:0x2800
	ds_read_b64_tr_b16 v[92:93], v78 offset:0x3000
	v_add_f32_e32 v79, v79, v177
	ds_read_b64_tr_b16 v[94:95], v78 offset:0x3800
	v_fmac_f32_e32 v79, v174, v97
	ds_read_b64_tr_b16 v[174:175], v78 offset:0x200
	ds_read_b64_tr_b16 v[176:177], v78 offset:0xa00
	ds_read_b64_tr_b16 v[182:183], v78 offset:0x1200
	ds_read_b64_tr_b16 v[184:185], v78 offset:0x1a00
	ds_read_b64_tr_b16 v[186:187], v78 offset:0x2200
	ds_read_b64_tr_b16 v[188:189], v78 offset:0x2a00
	ds_read_b64_tr_b16 v[190:191], v78 offset:0x3200
	ds_read_b64_tr_b16 v[192:193], v78 offset:0x3a00
	s_waitcnt lgkmcnt(8)
	v_permlane32_swap_b32_e32 v178, v180
	v_permlane32_swap_b32_e32 v179, v181
	v_permlane32_swap_b32_e32 v84, v86
	v_permlane32_swap_b32_e32 v85, v87
	v_permlane32_swap_b32_e32 v66, v68
	v_permlane32_swap_b32_e32 v67, v69
	v_permlane32_swap_b32_e32 v70, v72
	v_permlane32_swap_b32_e32 v71, v73
	v_mfma_f32_32x32x16_bf16 v[50:65], v[178:181], v[74:77], v[50:65]
	ds_read_b64_tr_b16 v[74:75], v78 offset:0x400
	ds_read_b64_tr_b16 v[76:77], v78 offset:0xc00
	v_mfma_f32_32x32x16_bf16 v[50:65], v[84:87], v[80:83], v[50:65]
	ds_read_b64_tr_b16 v[80:81], v78 offset:0x1400
	ds_read_b64_tr_b16 v[82:83], v78 offset:0x1c00
	v_mfma_f32_32x32x16_bf16 v[50:65], v[66:69], v[88:91], v[50:65]
	ds_read_b64_tr_b16 v[88:89], v78 offset:0x2400
	ds_read_b64_tr_b16 v[90:91], v78 offset:0x2c00
	v_mfma_f32_32x32x16_bf16 v[50:65], v[70:73], v[92:95], v[50:65]
	ds_read_b64_tr_b16 v[92:93], v78 offset:0x3400
	ds_read_b64_tr_b16 v[94:95], v78 offset:0x3c00
	s_waitcnt lgkmcnt(8)
	v_mfma_f32_32x32x16_bf16 v[34:49], v[178:181], v[174:177], v[34:49]
	ds_read_b64_tr_b16 v[174:175], v78 offset:0x600
	ds_read_b64_tr_b16 v[176:177], v78 offset:0xe00
	v_mfma_f32_32x32x16_bf16 v[34:49], v[84:87], v[182:185], v[34:49]
	ds_read_b64_tr_b16 v[182:183], v78 offset:0x1600
	ds_read_b64_tr_b16 v[184:185], v78 offset:0x1e00
	v_mfma_f32_32x32x16_bf16 v[34:49], v[66:69], v[186:189], v[34:49]
	ds_read_b64_tr_b16 v[186:187], v78 offset:0x2600
	ds_read_b64_tr_b16 v[188:189], v78 offset:0x2e00
	v_mfma_f32_32x32x16_bf16 v[34:49], v[70:73], v[190:193], v[34:49]
	ds_read_b64_tr_b16 v[190:191], v78 offset:0x3600
	ds_read_b64_tr_b16 v[192:193], v78 offset:0x3e00
	s_waitcnt lgkmcnt(8)
	v_mfma_f32_32x32x16_bf16 v[18:33], v[178:181], v[74:77], v[18:33]
	s_waitcnt lgkmcnt(0)
	v_mfma_f32_32x32x16_bf16 v[18:33], v[84:87], v[80:83], v[18:33]
	v_mfma_f32_32x32x16_bf16 v[18:33], v[66:69], v[88:91], v[18:33]
	v_mfma_f32_32x32x16_bf16 v[18:33], v[70:73], v[92:95], v[18:33]
	v_mfma_f32_32x32x16_bf16 v[2:17], v[178:181], v[174:177], v[2:17]
	s_add_i32 s86, s86, 64
	s_add_i32 s12, s12, 1
	s_add_u32 s94, s94, s16
	s_addc_u32 s95, s95, s17
	s_add_u32 s96, s96, s14
	s_addc_u32 s97, s97, s15


	v_mfma_f32_32x32x16_bf16 v[2:17], v[84:87], v[182:185], v[2:17]
	v_subrev_u32_e32 v168, 64, v168
	s_cmp_eq_u32 s83, s86
	v_mfma_f32_32x32x16_bf16 v[2:17], v[66:69], v[186:189], v[2:17]
	v_mfma_f32_32x32x16_bf16 v[2:17], v[70:73], v[190:193], v[2:17]
	s_cbranch_scc1 .LBB0_815
	v_mov_b32_e32 v174, v79
	s_add_i32 s56, s86, 0xe0
	s_cmp_ge_i32 s56, s84
	s_cbranch_scc0 .LBB0_805

.Latt1_drain_nodma:
	s_add_i32 s86, s86, 64
	s_add_i32 s12, s12, 1
	s_add_u32 s94, s94, s16
	s_addc_u32 s95, s95, s17
	s_add_u32 s96, s96, s14
	s_addc_u32 s97, s97, s15
	s_cmp_eq_u32 s83, s86
	s_cbranch_scc0 .Latt1_drain
	s_branch .LBB0_815

.LBB0_945:
	s_or_b64 exec, exec, s[0:1]
	s_lshl_b32 s55, s80, 8
	s_and_b32 s0, s81, 15
	s_add_i32 s55, s55, s63
	s_lshl_b32 s54, s0, 8
	v_mov_b32_e32 v168, v1
	s_ashr_i32 s0, s55, 31
	s_add_u32 s52, s52, s55
	v_and_b32_e32 v167, 31, v168
	v_or_b32_e32 v30, s52, v167
	v_mov_b64_e32 v[2:3], s[6:7]
	s_addc_u32 s53, s53, s0
	v_mad_u64_u32 v[2:3], s[0:1], v30, s68, v[2:3]
	v_bfe_u32 v169, v168, 5, 1
	v_mad_i32_i24 v3, s53, v162, v3
	s_lshl_b32 s12, s82, 1
	v_lshl_add_u64 v[2:3], v[2:3], 0, s[12:13]
	v_lshlrev_b32_e32 v148, 4, v169
	v_lshl_add_u64 v[44:45], v[2:3], 0, v[148:149]
	global_load_dwordx4 v[32:35], v[44:45], off
	global_load_dwordx4 v[36:39], v[44:45], off offset:32
	global_load_dwordx4 v[26:29], v[44:45], off offset:64
	global_load_dwordx4 v[22:25], v[44:45], off offset:96
	global_load_dwordx4 v[18:21], v[44:45], off offset:128
	global_load_dwordx4 v[14:17], v[44:45], off offset:160
	global_load_dwordx4 v[10:13], v[44:45], off offset:192
	v_and_b32_e32 v118, 32, v168
	global_load_dwordx4 v[6:9], v118, s[4:5] offset:576
	s_waitcnt lgkmcnt(0)
	global_load_dwordx4 v[2:5], v118, s[4:5] offset:592
	global_load_dwordx4 v[102:105], v118, s[4:5] offset:704
	global_load_dwordx4 v[110:113], v118, s[4:5] offset:720
	global_load_dwordx4 v[40:43], v[44:45], off offset:224
	global_load_dwordx4 v[82:85], v[44:45], off offset:256
	global_load_dwordx4 v[138:141], v[44:45], off offset:288
	global_load_dwordx4 v[70:73], v[44:45], off offset:320
	global_load_dwordx4 v[142:145], v[44:45], off offset:352
	v_mov_b32_e32 v31, s53
	s_mov_b32 m0, s71
	s_mov_b32 s12, 1
	s_waitcnt vmcnt(0)
	v_and_b32_e32 v191, 0xffff0000, v32
	v_lshlrev_b32_e32 v190, 16, v32
	v_lshlrev_b32_e32 v206, 16, v26
	v_and_b32_e32 v207, 0xffff0000, v26
	v_lshlrev_b32_e32 v208, 16, v27
	v_and_b32_e32 v209, 0xffff0000, v27
	v_lshlrev_b32_e32 v210, 16, v28
	v_and_b32_e32 v211, 0xffff0000, v28
	v_lshlrev_b32_e32 v212, 16, v29
	v_and_b32_e32 v213, 0xffff0000, v29
	v_lshlrev_b32_e32 v222, 16, v18
	v_and_b32_e32 v223, 0xffff0000, v18
	v_lshlrev_b32_e32 v224, 16, v19
	v_and_b32_e32 v225, 0xffff0000, v19
	v_lshlrev_b32_e32 v226, 16, v20
	v_and_b32_e32 v227, 0xffff0000, v20
	v_lshlrev_b32_e32 v228, 16, v21
	v_and_b32_e32 v229, 0xffff0000, v21
	global_load_dwordx4 v[26:29], v118, s[4:5] offset:640
	global_load_dwordx4 v[156:159], v118, s[4:5] offset:656
	global_load_dwordx4 v[18:21], v118, s[4:5] offset:528
	v_mul_f32_e32 v188, v191, v191
	v_lshlrev_b32_e32 v192, 16, v33
	v_fmac_f32_e32 v188, v190, v190
	v_and_b32_e32 v193, 0xffff0000, v33
	v_fmac_f32_e32 v188, v192, v192
	v_lshlrev_b32_e32 v194, 16, v34
	v_fmac_f32_e32 v188, v193, v193
	v_and_b32_e32 v195, 0xffff0000, v34
	v_fmac_f32_e32 v188, v194, v194
	v_lshlrev_b32_e32 v196, 16, v35
	v_fmac_f32_e32 v188, v195, v195
	v_and_b32_e32 v197, 0xffff0000, v35
	v_fmac_f32_e32 v188, v196, v196
	v_lshlrev_b32_e32 v198, 16, v36
	v_fmac_f32_e32 v188, v197, v197
	v_and_b32_e32 v199, 0xffff0000, v36
	v_fmac_f32_e32 v188, v198, v198
	v_lshlrev_b32_e32 v200, 16, v37
	v_lshlrev_b32_e32 v214, 16, v22
	v_and_b32_e32 v215, 0xffff0000, v22
	v_lshlrev_b32_e32 v216, 16, v23
	v_and_b32_e32 v217, 0xffff0000, v23
	v_lshlrev_b32_e32 v218, 16, v24
	v_and_b32_e32 v219, 0xffff0000, v24
	v_lshlrev_b32_e32 v220, 16, v25
	v_and_b32_e32 v221, 0xffff0000, v25
	v_fmac_f32_e32 v188, v199, v199
	global_load_dwordx4 v[22:25], v118, s[4:5] offset:512
	v_and_b32_e32 v201, 0xffff0000, v37
	v_fmac_f32_e32 v188, v200, v200
	v_lshlrev_b32_e32 v202, 16, v38
	v_fmac_f32_e32 v188, v201, v201
	v_and_b32_e32 v203, 0xffff0000, v38
	v_fmac_f32_e32 v188, v202, v202
	v_lshlrev_b32_e32 v204, 16, v39
	v_fmac_f32_e32 v188, v203, v203
	v_and_b32_e32 v205, 0xffff0000, v39
	v_fmac_f32_e32 v188, v204, v204
	v_fmac_f32_e32 v188, v205, v205
	v_fmac_f32_e32 v188, v206, v206
	v_fmac_f32_e32 v188, v207, v207
	v_fmac_f32_e32 v188, v208, v208
	v_fmac_f32_e32 v188, v209, v209
	v_fmac_f32_e32 v188, v210, v210
	v_fmac_f32_e32 v188, v211, v211
	v_fmac_f32_e32 v188, v212, v212
	v_fmac_f32_e32 v188, v213, v213
	v_fmac_f32_e32 v188, v214, v214
	v_fmac_f32_e32 v188, v215, v215
	v_fmac_f32_e32 v188, v216, v216
	v_fmac_f32_e32 v188, v217, v217
	v_fmac_f32_e32 v188, v218, v218
	v_fmac_f32_e32 v188, v219, v219
	v_fmac_f32_e32 v188, v220, v220
	v_fmac_f32_e32 v188, v221, v221
	v_fmac_f32_e32 v188, v222, v222
	v_fmac_f32_e32 v188, v223, v223
	v_fmac_f32_e32 v188, v224, v224
	v_fmac_f32_e32 v188, v225, v225
	v_fmac_f32_e32 v188, v226, v226
	v_fmac_f32_e32 v188, v227, v227
	v_fmac_f32_e32 v188, v228, v228
	v_lshlrev_b32_e32 v230, 16, v14
	v_fmac_f32_e32 v188, v229, v229
	v_and_b32_e32 v231, 0xffff0000, v14
	v_fmac_f32_e32 v188, v230, v230
	v_lshlrev_b32_e32 v232, 16, v15
	v_fmac_f32_e32 v188, v231, v231
	v_and_b32_e32 v233, 0xffff0000, v15
	v_fmac_f32_e32 v188, v232, v232
	v_lshlrev_b32_e32 v234, 16, v16
	v_fmac_f32_e32 v188, v233, v233
	v_and_b32_e32 v235, 0xffff0000, v16
	v_fmac_f32_e32 v188, v234, v234
	v_lshlrev_b32_e32 v246, 16, v40
	v_and_b32_e32 v247, 0xffff0000, v40
	v_lshlrev_b32_e32 v248, 16, v41
	v_and_b32_e32 v249, 0xffff0000, v41
	v_lshlrev_b32_e32 v250, 16, v42
	v_and_b32_e32 v251, 0xffff0000, v42
	v_lshlrev_b32_e32 v252, 16, v43
	v_and_b32_e32 v253, 0xffff0000, v43
	global_load_dwordx4 v[106:109], v118, s[4:5] offset:16
	global_load_dwordx4 v[114:117], v118, s[4:5]
	global_load_dwordx4 v[94:97], v118, s[4:5] offset:80
	global_load_dwordx4 v[98:101], v118, s[4:5] offset:64
	global_load_dwordx4 v[86:89], v118, s[4:5] offset:144
	global_load_dwordx4 v[90:93], v118, s[4:5] offset:128
	global_load_dwordx4 v[74:77], v118, s[4:5] offset:208
	global_load_dwordx4 v[78:81], v118, s[4:5] offset:192
	global_load_dwordx4 v[62:65], v118, s[4:5] offset:272
	global_load_dwordx4 v[66:69], v118, s[4:5] offset:256
	global_load_dwordx4 v[54:57], v118, s[4:5] offset:336
	global_load_dwordx4 v[58:61], v118, s[4:5] offset:320
	global_load_dwordx4 v[46:49], v118, s[4:5] offset:400
	global_load_dwordx4 v[50:53], v118, s[4:5] offset:384
	global_load_dwordx4 v[38:41], v118, s[4:5] offset:464
	global_load_dwordx4 v[42:45], v118, s[4:5] offset:448
	v_lshlrev_b32_e32 v236, 16, v17
	v_fmac_f32_e32 v188, v235, v235
	v_and_b32_e32 v237, 0xffff0000, v17
	v_fmac_f32_e32 v188, v236, v236
	v_lshlrev_b32_e32 v238, 16, v10
	v_fmac_f32_e32 v188, v237, v237
	v_and_b32_e32 v239, 0xffff0000, v10
	v_fmac_f32_e32 v188, v238, v238
	v_lshlrev_b32_e32 v240, 16, v11
	v_fmac_f32_e32 v188, v239, v239
	v_and_b32_e32 v241, 0xffff0000, v11
	v_fmac_f32_e32 v188, v240, v240
	v_lshlrev_b32_e32 v242, 16, v12
	v_fmac_f32_e32 v188, v241, v241
	v_and_b32_e32 v243, 0xffff0000, v12
	v_fmac_f32_e32 v188, v242, v242
	v_lshlrev_b32_e32 v244, 16, v13
	v_fmac_f32_e32 v188, v243, v243
	v_and_b32_e32 v245, 0xffff0000, v13
	v_fmac_f32_e32 v188, v244, v244
	v_fmac_f32_e32 v188, v245, v245
	v_fmac_f32_e32 v188, v246, v246
	v_fmac_f32_e32 v188, v247, v247
	v_fmac_f32_e32 v188, v248, v248
	v_fmac_f32_e32 v188, v249, v249
	v_fmac_f32_e32 v188, v250, v250
	v_fmac_f32_e32 v188, v251, v251
	v_fmac_f32_e32 v188, v252, v252
	v_lshlrev_b32_e32 v187, 16, v82
	v_lshlrev_b32_e32 v186, 16, v70
	v_fmac_f32_e32 v188, v253, v253
	v_lshlrev_b32_e32 v124, 16, v144
	v_and_b32_e32 v126, 0xffff0000, v144
	v_lshlrev_b32_e32 v131, 16, v139
	v_and_b32_e32 v133, 0xffff0000, v139
	v_lshlrev_b32_e32 v137, 16, v138
	v_lshlrev_b32_e32 v136, 16, v142
	v_and_b32_e32 v139, 0xffff0000, v138
	v_and_b32_e32 v138, 0xffff0000, v142
	v_lshlrev_b32_e32 v142, 16, v73
	v_and_b32_e32 v144, 0xffff0000, v73
	v_lshlrev_b32_e32 v152, 16, v72
	v_and_b32_e32 v154, 0xffff0000, v72
	v_pk_mul_f32 v[72:73], v[186:187], v[186:187]
	s_waitcnt vmcnt(18)
	v_mov_b32_e32 v150, v158
	v_mov_b32_e32 v158, v156
	v_lshlrev_b32_e32 v156, 16, v71
	v_and_b32_e32 v184, 0xffff0000, v71
	v_and_b32_e32 v189, 0xffff0000, v82
	v_add_f32_e32 v71, v73, v188
	v_and_b32_e32 v188, 0xffff0000, v70
	v_mov_b32_e32 v128, v110
	v_mov_b32_e32 v129, v2
	v_mov_b32_e32 v2, v111
	s_waitcnt vmcnt(17)
	v_mov_b32_e32 v151, v20
	v_mov_b32_e32 v20, v159
	v_mov_b32_e32 v159, v18
	v_mov_b32_e32 v18, v157
	v_lshlrev_b32_e32 v157, 16, v83
	v_pk_mul_f32 v[110:111], v[188:189], v[188:189]
	v_lshlrev_b32_e32 v119, 16, v141
	v_and_b32_e32 v121, 0xffff0000, v141
	v_lshlrev_b32_e32 v125, 16, v140
	v_and_b32_e32 v127, 0xffff0000, v140
	v_mov_b32_e32 v140, v102
	v_mov_b32_e32 v141, v6
	v_mov_b32_e32 v6, v103
	v_pk_mul_f32 v[102:103], v[156:157], v[156:157]
	v_and_b32_e32 v185, 0xffff0000, v83
	v_add_f32_e32 v70, v111, v71
	v_mov_b32_e32 v134, v104
	v_mov_b32_e32 v135, v8
	v_mov_b32_e32 v8, v105
	v_lshlrev_b32_e32 v153, 16, v84
	v_pk_mul_f32 v[104:105], v[184:185], v[184:185]
	v_add_f32_e32 v70, v103, v70
	v_pk_mul_f32 v[180:181], v[152:153], v[152:153]
	v_and_b32_e32 v155, 0xffff0000, v84
	v_add_f32_e32 v70, v105, v70
	v_lshlrev_b32_e32 v130, 16, v143
	v_and_b32_e32 v132, 0xffff0000, v143
	v_lshlrev_b32_e32 v143, 16, v85
	v_pk_mul_f32 v[182:183], v[154:155], v[154:155]
	v_add_f32_e32 v70, v181, v70
	v_lshlrev_b32_e32 v118, 16, v145
	v_and_b32_e32 v120, 0xffff0000, v145
	v_pk_mul_f32 v[176:177], v[142:143], v[142:143]
	v_and_b32_e32 v145, 0xffff0000, v85
	v_add_f32_e32 v70, v183, v70
	v_pk_mul_f32 v[178:179], v[144:145], v[144:145]
	v_add_f32_e32 v70, v177, v70
	v_pk_mul_f32 v[172:173], v[136:137], v[136:137]
	v_add_f32_e32 v70, v179, v70
	v_pk_mul_f32 v[174:175], v[138:139], v[138:139]
	v_add_f32_e32 v70, v173, v70
	v_add_f32_e32 v70, v175, v70
	v_fmac_f32_e32 v70, v131, v131
	v_fmac_f32_e32 v70, v133, v133
	v_fmac_f32_e32 v70, v125, v125
	v_fmac_f32_e32 v70, v127, v127
	v_fmac_f32_e32 v70, v119, v119
	v_fmac_f32_e32 v70, v121, v121
	v_add_f32_e32 v103, v72, v70
	v_add_f32_e32 v103, v110, v103
	v_add_f32_e32 v102, v102, v103
	v_add_f32_e32 v173, v104, v102
	v_add_f32_e32 v173, v180, v173
	v_add_f32_e32 v173, v182, v173
	v_add_f32_e32 v173, v176, v173
	v_add_f32_e32 v173, v178, v173
	v_mov_b32_e32 v176, v132
	v_mov_b32_e32 v177, v130
	s_waitcnt vmcnt(16)
	v_mov_b32_e32 v179, v24
	v_add_f32_e32 v24, v172, v173
	v_lshlrev_b64 v[10:11], 8, v[30:31]
	v_pk_mul_f32 v[176:177], v[176:177], v[176:177]
	v_add_f32_e32 v24, v174, v24
	v_lshl_add_u64 v[10:11], s[10:11], 0, v[10:11]
	v_lshlrev_b32_e32 v12, 6, v169
	v_mov_b32_e32 v13, v149
	v_mov_b32_e32 v180, v126
	v_mov_b32_e32 v181, v124
	v_add_f32_e32 v24, v177, v24
	v_lshl_add_u64 v[170:171], v[10:11], 0, v[12:13]
	v_pk_mul_f32 v[180:181], v[180:181], v[180:181]
	v_add_f32_e32 v24, v176, v24
	global_load_dwordx4 v[10:13], v[170:171], off offset:48
	global_load_dwordx4 v[14:17], v[170:171], off offset:32
	global_load_dwordx4 v[30:33], v[170:171], off offset:16
	global_load_dwordx4 v[34:37], v[170:171], off
	v_mov_b32_e32 v122, v112
	v_mov_b32_e32 v123, v4
	v_mov_b32_e32 v4, v113
	global_load_dwordx4 v[70:73], v[170:171], off offset:176
	global_load_dwordx4 v[82:85], v[170:171], off offset:160
	global_load_dwordx4 v[102:105], v[170:171], off offset:144
	global_load_dwordx4 v[110:113], v[170:171], off offset:128
	v_mov_b32_e32 v170, v120
	v_mov_b32_e32 v171, v118
	v_add_f32_e32 v24, v181, v24
	v_pk_mul_f32 v[170:171], v[170:171], v[170:171]
	v_add_f32_e32 v24, v180, v24
	v_add_f32_e32 v24, v171, v24
	v_add_f32_e32 v24, v170, v24
	v_mov_b32_e32 v178, v28
	v_mov_b32_e32 v28, v24
	s_nop 1
	v_permlane32_swap_b32_e32 v24, v28
	v_add_f32_e32 v24, v24, v28
	v_fmamk_f32 v24, v24, 0x3baaaaab, v163
	v_mul_f32_e32 v28, 0x4b800000, v24
	v_cmp_gt_f32_e32 vcc, s69, v24
	s_nop 1
	v_cndmask_b32_e32 v24, v24, v28, vcc
	v_rsq_f32_e32 v170, v24
	v_mov_b32_e32 v24, v29
	v_mov_b32_e32 v29, v22
	v_mov_b32_e32 v28, v26
	v_mul_f32_e32 v22, 0x45800000, v170
	v_cndmask_b32_e32 v22, v170, v22, vcc
	v_mul_f32_e32 v26, 0x3dd53b94, v22
	s_waitcnt vmcnt(22)
	v_mul_f32_e32 v22, v114, v26
	v_mul_f32_e32 v114, v22, v190
	v_mul_f32_e32 v22, v106, v26
	v_mul_f32_e32 v106, v22, v194
	v_mul_f32_e32 v22, v115, v26
	v_mul_f32_e32 v115, v22, v191
	v_mul_f32_e32 v22, v107, v26
	v_mul_f32_e32 v107, v22, v195
	v_mul_f32_e32 v22, v116, v26
	v_mul_f32_e32 v116, v22, v192
	v_mul_f32_e32 v22, v108, v26
	v_mul_f32_e32 v108, v22, v196
	v_mul_f32_e32 v22, v117, v26
	v_mul_f32_e32 v117, v22, v193
	v_mul_f32_e32 v22, v109, v26
	v_mul_f32_e32 v109, v22, v197
	s_waitcnt vmcnt(20)
	v_mul_f32_e32 v22, v98, v26
	v_mul_f32_e32 v170, v22, v198
	v_mul_f32_e32 v22, v94, v26
	v_mul_f32_e32 v94, v22, v202
	v_mul_f32_e32 v22, v99, v26
	v_mul_f32_e32 v171, v22, v199
	v_mul_f32_e32 v22, v95, v26
	v_mul_f32_e32 v95, v22, v203
	v_mul_f32_e32 v22, v100, v26
	v_mul_f32_e32 v172, v22, v200
	v_mul_f32_e32 v22, v96, v26
	v_mul_f32_e32 v96, v22, v204
	v_mul_f32_e32 v22, v101, v26
	v_mul_f32_e32 v173, v22, v201
	v_mul_f32_e32 v22, v97, v26
	v_mul_f32_e32 v97, v22, v205
	s_waitcnt vmcnt(18)
	v_mul_f32_e32 v22, v90, v26
	v_mul_f32_e32 v90, v22, v206
	v_mul_f32_e32 v22, v86, v26
	v_mul_f32_e32 v86, v22, v210
	v_mul_f32_e32 v22, v91, v26
	v_mul_f32_e32 v91, v22, v207
	v_mul_f32_e32 v22, v87, v26
	v_mul_f32_e32 v87, v22, v211
	v_mul_f32_e32 v22, v92, v26
	v_mul_f32_e32 v92, v22, v208
	v_mul_f32_e32 v22, v88, v26
	v_mul_f32_e32 v88, v22, v212
	v_mul_f32_e32 v22, v93, v26
	v_mul_f32_e32 v93, v22, v209
	v_mul_f32_e32 v22, v89, v26
	v_mul_f32_e32 v89, v22, v213
	s_waitcnt vmcnt(16)
	v_mul_f32_e32 v22, v78, v26
	v_mul_f32_e32 v78, v22, v214
	v_mul_f32_e32 v22, v74, v26
	v_mul_f32_e32 v74, v22, v218
	v_mul_f32_e32 v22, v79, v26
	v_mul_f32_e32 v79, v22, v215
	v_mul_f32_e32 v22, v75, v26
	v_mul_f32_e32 v75, v22, v219
	v_mul_f32_e32 v22, v80, v26
	v_mul_f32_e32 v80, v22, v216
	v_mul_f32_e32 v22, v76, v26
	v_mul_f32_e32 v76, v22, v220
	v_mul_f32_e32 v22, v81, v26
	v_mul_f32_e32 v81, v22, v217
	v_mul_f32_e32 v22, v77, v26
	v_mul_f32_e32 v77, v22, v221
	s_waitcnt vmcnt(14)
	v_mul_f32_e32 v22, v66, v26
	v_mul_f32_e32 v66, v22, v222
	v_mul_f32_e32 v22, v26, v62
	v_mul_f32_e32 v62, v22, v226
	v_mul_f32_e32 v22, v67, v26
	v_mul_f32_e32 v67, v22, v223
	v_mul_f32_e32 v22, v26, v63
	v_mul_f32_e32 v63, v22, v227
	v_mul_f32_e32 v22, v68, v26
	v_mul_f32_e32 v68, v22, v224
	v_mul_f32_e32 v22, v26, v64
	v_mul_f32_e32 v64, v22, v228
	v_mul_f32_e32 v22, v69, v26
	v_mul_f32_e32 v69, v22, v225
	v_mul_f32_e32 v22, v26, v65
	v_mul_f32_e32 v65, v22, v229
	s_waitcnt vmcnt(12)
	v_mul_f32_e32 v22, v26, v58
	v_mul_f32_e32 v58, v22, v230
	v_mul_f32_e32 v22, v26, v54
	v_mul_f32_e32 v54, v22, v234
	v_mul_f32_e32 v22, v26, v59
	v_mul_f32_e32 v59, v22, v231
	v_mul_f32_e32 v22, v26, v55
	v_mul_f32_e32 v55, v22, v235
	v_mul_f32_e32 v22, v26, v60
	v_mul_f32_e32 v60, v22, v232
	v_mul_f32_e32 v22, v26, v56
	v_mul_f32_e32 v56, v22, v236
	v_mul_f32_e32 v22, v26, v61
	v_mul_f32_e32 v61, v22, v233
	v_mul_f32_e32 v22, v26, v57
	v_mul_f32_e32 v57, v22, v237
	s_waitcnt vmcnt(10)
	v_mul_f32_e32 v22, v26, v50
	v_mul_f32_e32 v174, v22, v238
	v_mul_f32_e32 v22, v26, v46
	v_mul_f32_e32 v175, v22, v242
	v_mul_f32_e32 v22, v26, v51
	v_mul_f32_e32 v176, v22, v239
	v_mul_f32_e32 v22, v26, v47
	v_mul_f32_e32 v177, v22, v243
	v_mul_f32_e32 v22, v26, v52
	v_mul_f32_e32 v52, v22, v240
	v_mul_f32_e32 v22, v26, v48
	v_mul_f32_e32 v180, v22, v244
	v_mul_f32_e32 v22, v26, v53
	v_mul_f32_e32 v53, v22, v241
	v_mul_f32_e32 v22, v26, v49
	v_mul_f32_e32 v181, v22, v245
	s_waitcnt vmcnt(8)
	v_mul_f32_e32 v22, v26, v42
	v_mul_f32_e32 v182, v22, v246
	v_mul_f32_e32 v22, v26, v38
	v_mul_f32_e32 v183, v22, v250
	v_mul_f32_e32 v22, v26, v43
	v_mul_f32_e32 v190, v22, v247
	v_mul_f32_e32 v22, v26, v39
	v_mul_f32_e32 v191, v22, v251
	v_mul_f32_e32 v22, v26, v44
	v_mul_f32_e32 v192, v22, v248
	v_mul_f32_e32 v22, v26, v40
	v_mul_f32_e32 v193, v22, v252
	v_mul_f32_e32 v22, v26, v45
	v_mul_f32_e32 v194, v22, v249
	v_mul_f32_e32 v22, v26, v41
	v_pk_mul_f32 v[28:29], v[26:27], v[28:29] op_sel_hi:[0,1]
	v_mul_f32_e32 v195, v22, v253
	v_pk_mul_f32 v[28:29], v[28:29], v[186:187]
	v_mov_b32_e32 v22, v27
	v_pk_mul_f32 v[38:39], v[26:27], v[158:159] op_sel_hi:[0,1]
	v_pk_mul_f32 v[22:23], v[26:27], v[22:23] op_sel_hi:[0,1]
	v_pk_mul_f32 v[18:19], v[26:27], v[18:19] op_sel_hi:[0,1]
	v_pk_mul_f32 v[40:41], v[26:27], v[178:179] op_sel_hi:[0,1]
	v_pk_mul_f32 v[42:43], v[26:27], v[150:151] op_sel_hi:[0,1]
	v_pk_mul_f32 v[24:25], v[26:27], v[24:25] op_sel_hi:[0,1]
	v_pk_mul_f32 v[20:21], v[26:27], v[20:21] op_sel_hi:[0,1]
	v_pk_mul_f32 v[44:45], v[26:27], v[140:141] op_sel_hi:[0,1]
	v_pk_mul_f32 v[46:47], v[26:27], v[128:129] op_sel_hi:[0,1]
	v_pk_mul_f32 v[6:7], v[26:27], v[6:7] op_sel_hi:[0,1]
	v_pk_mul_f32 v[2:3], v[26:27], v[2:3] op_sel_hi:[0,1]
	v_pk_mul_f32 v[48:49], v[26:27], v[134:135] op_sel_hi:[0,1]
	v_pk_mul_f32 v[50:51], v[26:27], v[122:123] op_sel_hi:[0,1]
	v_pk_mul_f32 v[8:9], v[26:27], v[8:9] op_sel_hi:[0,1]
	v_pk_mul_f32 v[4:5], v[26:27], v[4:5] op_sel_hi:[0,1]
	s_waitcnt vmcnt(4)
	v_pk_mul_f32 v[26:27], v[28:29], v[34:35] op_sel:[1,0] op_sel_hi:[0,1]
	v_pk_mul_f32 v[22:23], v[22:23], v[188:189]
	v_pk_mul_f32 v[48:49], v[48:49], v[130:131]
	v_sub_f32_e32 v130, v26, v27
	v_pk_mul_f32 v[26:27], v[28:29], v[34:35]
	v_pk_mul_f32 v[40:41], v[40:41], v[156:157]
	v_add_f32_e32 v28, v27, v26
	v_pk_mul_f32 v[26:27], v[22:23], v[36:37] op_sel:[1,0] op_sel_hi:[0,1]
	v_pk_mul_f32 v[22:23], v[22:23], v[36:37]
	v_sub_f32_e32 v26, v26, v27
	v_add_f32_e32 v27, v23, v22
	v_pk_mul_f32 v[22:23], v[40:41], v[30:31] op_sel:[1,0] op_sel_hi:[0,1]
	v_pk_mul_f32 v[24:25], v[24:25], v[184:185]
	v_sub_f32_e32 v29, v22, v23
	v_pk_mul_f32 v[22:23], v[40:41], v[30:31]
	v_pk_mul_f32 v[38:39], v[38:39], v[152:153]
	v_add_f32_e32 v30, v23, v22
	v_pk_mul_f32 v[22:23], v[24:25], v[32:33] op_sel:[1,0] op_sel_hi:[0,1]
	v_sub_f32_e32 v31, v22, v23
	v_pk_mul_f32 v[22:23], v[24:25], v[32:33]
	v_pk_mul_f32 v[18:19], v[18:19], v[154:155]
	v_add_f32_e32 v24, v23, v22
	v_pk_mul_f32 v[22:23], v[38:39], v[14:15] op_sel:[1,0] op_sel_hi:[0,1]
	v_pk_mul_f32 v[14:15], v[38:39], v[14:15]
	v_sub_f32_e32 v22, v22, v23
	v_add_f32_e32 v23, v15, v14
	v_pk_mul_f32 v[14:15], v[18:19], v[16:17] op_sel:[1,0] op_sel_hi:[0,1]
	v_pk_mul_f32 v[42:43], v[42:43], v[142:143]
	v_sub_f32_e32 v25, v14, v15
	v_pk_mul_f32 v[14:15], v[18:19], v[16:17]
	v_pk_mul_f32 v[20:21], v[20:21], v[144:145]
	v_add_f32_e32 v16, v15, v14
	v_pk_mul_f32 v[14:15], v[42:43], v[10:11] op_sel:[1,0] op_sel_hi:[0,1]
	v_pk_mul_f32 v[10:11], v[42:43], v[10:11]
	v_sub_f32_e32 v14, v14, v15
	v_add_f32_e32 v15, v11, v10
	v_pk_mul_f32 v[10:11], v[20:21], v[12:13] op_sel:[1,0] op_sel_hi:[0,1]
	v_pk_mul_f32 v[44:45], v[44:45], v[136:137]
	v_sub_f32_e32 v17, v10, v11
	v_pk_mul_f32 v[10:11], v[20:21], v[12:13]
	v_pk_mul_f32 v[6:7], v[6:7], v[138:139]
	v_add_f32_e32 v12, v11, v10
	s_waitcnt vmcnt(0)
	v_pk_mul_f32 v[10:11], v[44:45], v[110:111] op_sel:[1,0] op_sel_hi:[0,1]
	v_sub_f32_e32 v13, v10, v11
	v_pk_mul_f32 v[10:11], v[44:45], v[110:111]
	v_pk_mul_f32 v[8:9], v[8:9], v[132:133]
	v_add_f32_e32 v18, v11, v10
	v_pk_mul_f32 v[10:11], v[6:7], v[112:113] op_sel:[1,0] op_sel_hi:[0,1]
	v_pk_mul_f32 v[6:7], v[6:7], v[112:113]
	v_sub_f32_e32 v10, v10, v11
	v_add_f32_e32 v11, v7, v6
	v_pk_mul_f32 v[6:7], v[48:49], v[102:103] op_sel:[1,0] op_sel_hi:[0,1]
	v_sub_f32_e32 v19, v6, v7
	v_pk_mul_f32 v[6:7], v[48:49], v[102:103]
	v_pk_mul_f32 v[46:47], v[46:47], v[124:125]
	v_add_f32_e32 v20, v7, v6
	v_pk_mul_f32 v[6:7], v[8:9], v[104:105] op_sel:[1,0] op_sel_hi:[0,1]
	v_sub_f32_e32 v21, v6, v7
	v_pk_mul_f32 v[6:7], v[8:9], v[104:105]
	v_pk_mul_f32 v[2:3], v[2:3], v[126:127]
	v_add_f32_e32 v8, v7, v6
	v_pk_mul_f32 v[6:7], v[46:47], v[82:83] op_sel:[1,0] op_sel_hi:[0,1]
	v_sub_f32_e32 v9, v6, v7
	v_pk_mul_f32 v[6:7], v[46:47], v[82:83]
	v_pk_mul_f32 v[50:51], v[50:51], v[118:119]
	v_add_f32_e32 v32, v7, v6
	v_pk_mul_f32 v[6:7], v[2:3], v[84:85] op_sel:[1,0] op_sel_hi:[0,1]
	v_pk_mul_f32 v[2:3], v[2:3], v[84:85]
	v_sub_f32_e32 v6, v6, v7
	v_add_f32_e32 v7, v3, v2
	v_pk_mul_f32 v[2:3], v[50:51], v[70:71] op_sel:[1,0] op_sel_hi:[0,1]
	v_pk_mul_f32 v[4:5], v[4:5], v[120:121]
	v_sub_f32_e32 v33, v2, v3
	v_pk_mul_f32 v[2:3], v[50:51], v[70:71]
	v_cvt_pk_bf16_f32 v98, v114, v115
	v_cvt_pk_bf16_f32 v99, v116, v117
	v_cvt_pk_bf16_f32 v100, v106, v107
	v_cvt_pk_bf16_f32 v101, v108, v109
	v_cvt_pk_bf16_f32 v102, v170, v171
	s_nop 0
	v_add_f32_e32 v34, v3, v2
	v_pk_mul_f32 v[2:3], v[4:5], v[72:73] op_sel:[1,0] op_sel_hi:[0,1]
	v_sub_f32_e32 v35, v2, v3
	v_pk_mul_f32 v[2:3], v[4:5], v[72:73]
	v_cvt_pk_bf16_f32 v103, v172, v173
	v_cvt_pk_bf16_f32 v104, v94, v95
	v_cvt_pk_bf16_f32 v105, v96, v97
	v_cvt_pk_bf16_f32 v106, v90, v91
	v_cvt_pk_bf16_f32 v107, v92, v93
	s_nop 0
	v_add_f32_e32 v2, v3, v2
	v_cvt_pk_bf16_f32 v108, v86, v87
	v_cvt_pk_bf16_f32 v109, v88, v89
	v_cvt_pk_bf16_f32 v110, v78, v79
	v_cvt_pk_bf16_f32 v111, v80, v81
	v_cvt_pk_bf16_f32 v112, v74, v75
	v_cvt_pk_bf16_f32 v113, v76, v77
	v_cvt_pk_bf16_f32 v114, v66, v67
	v_cvt_pk_bf16_f32 v115, v68, v69
	v_cvt_pk_bf16_f32 v116, v62, v63
	v_cvt_pk_bf16_f32 v117, v64, v65
	v_cvt_pk_bf16_f32 v118, v58, v59
	v_cvt_pk_bf16_f32 v119, v60, v61
	v_cvt_pk_bf16_f32 v120, v54, v55
	v_cvt_pk_bf16_f32 v121, v56, v57
	v_cvt_pk_bf16_f32 v122, v174, v176
	v_cvt_pk_bf16_f32 v123, v52, v53
	v_cvt_pk_bf16_f32 v124, v175, v177
	v_cvt_pk_bf16_f32 v125, v180, v181
	v_cvt_pk_bf16_f32 v126, v182, v190
	v_cvt_pk_bf16_f32 v127, v192, v194
	v_cvt_pk_bf16_f32 v128, v183, v191
	v_cvt_pk_bf16_f32 v129, v193, v195
	v_cvt_pk_bf16_f32 v130, v130, v26
	v_cvt_pk_bf16_f32 v131, v29, v31
	v_cvt_pk_bf16_f32 v132, v22, v25
	v_cvt_pk_bf16_f32 v133, v14, v17
	v_cvt_pk_bf16_f32 v134, v13, v10
	v_cvt_pk_bf16_f32 v135, v19, v21
	v_cvt_pk_bf16_f32 v136, v9, v6
	v_cvt_pk_bf16_f32 v137, v33, v35
	v_cvt_pk_bf16_f32 v138, v28, v27
	v_cvt_pk_bf16_f32 v139, v30, v24
	v_cvt_pk_bf16_f32 v140, v23, v16
	v_cvt_pk_bf16_f32 v141, v15, v12
	v_cvt_pk_bf16_f32 v142, v18, v11
	v_cvt_pk_bf16_f32 v143, v20, v8
	v_cvt_pk_bf16_f32 v144, v32, v7
	v_cvt_pk_bf16_f32 v145, v34, v2
	v_mul_hi_i32 v2, v168, s70
	v_lshrrev_b32_e32 v3, 31, v2
	v_ashrrev_i32_e32 v2, 2, v2
	v_add_u32_e32 v2, v2, v3
	v_mul_lo_u32 v3, v2, 24
	v_sub_u32_e32 v3, v168, v3
	v_lshrrev_b32_e32 v16, 1, v2
	v_bitop3_b32 v3, v16, v3, 7 bitop3:0x6c
	v_mul_lo_u32 v2, v2, s68
	v_lshl_add_u32 v2, v3, 4, v2
	v_add_u32_e32 v3, 0x200, v168
	v_mul_hi_i32 v4, v3, s70
	v_lshrrev_b32_e32 v5, 31, v4
	v_ashrrev_i32_e32 v4, 2, v4
	v_add_u32_e32 v4, v4, v5
	v_mul_lo_u32 v5, v4, 24
	v_sub_u32_e32 v5, v3, v5
	v_lshrrev_b32_e32 v16, 1, v4
	v_bitop3_b32 v5, v16, v5, 7 bitop3:0x6c
	v_mul_lo_u32 v4, v4, s68
	v_lshl_add_u32 v4, v5, 4, v4
	v_add_u32_e32 v5, 0x400, v168
	v_mul_hi_i32 v6, v5, s70
	v_lshrrev_b32_e32 v7, 31, v6
	v_ashrrev_i32_e32 v6, 2, v6
	v_add_u32_e32 v6, v6, v7
	v_mul_lo_u32 v7, v6, 24
	v_sub_u32_e32 v5, v5, v7
	v_lshrrev_b32_e32 v16, 1, v6
	v_bitop3_b32 v5, v16, v5, 7 bitop3:0x6c
	v_mul_lo_u32 v6, v6, s68
	v_ashrrev_i32_e32 v9, 4, v168
	v_lshl_add_u32 v6, v5, 4, v6
	v_bfe_u32 v5, v168, 2, 2
	v_lshrrev_b32_e32 v7, 1, v168
	v_and_b32_e32 v10, 0x1ffff0, v9
	v_lshrrev_b32_e32 v9, 1, v9
	v_ashrrev_i32_e32 v3, 4, v3
	v_and_or_b32 v5, v7, 8, v5
	v_and_b32_e32 v7, 0x60, v168
	v_lshlrev_b32_e32 v8, 3, v168
	v_and_b32_e32 v9, 4, v9
	v_and_b32_e32 v11, 0x1ffff0, v3
	v_lshrrev_b32_e32 v3, 1, v3
	v_and_or_b32 v7, v8, 24, v7
	v_or3_b32 v9, v10, v9, v5
	v_and_b32_e32 v3, 4, v3
	s_barrier
	global_load_lds_dwordx4 v2, s[44:45]
	s_mov_b32 m0, s72
	v_lshlrev_b32_e32 v7, 1, v7
	v_lshlrev_b32_e32 v10, 11, v9
	v_or3_b32 v3, v11, v3, v5
	global_load_lds_dwordx4 v4, s[44:45]
	s_mov_b32 m0, s73
	v_or_b32_e32 v9, v10, v7
	v_lshlrev_b32_e32 v11, 11, v3
	global_load_lds_dwordx4 v6, s[44:45]
	s_mov_b32 m0, s64
	v_or_b32_e32 v3, v11, v7
	global_load_lds_dwordx4 v9, s[46:47]
	s_mov_b32 m0, s74
	v_lshlrev_b32_e32 v13, 1, v168
	global_load_lds_dwordx4 v3, s[46:47]
	v_lshlrev_b32_e32 v9, 4, v168
	v_and_b32_e32 v14, 32, v13
	v_or_b32_e32 v3, 32, v148
	v_mul_u32_u24_e32 v5, 0x180, v167
	v_and_b32_e32 v7, 0x70, v8
	v_and_b32_e32 v12, 0xc0, v9
	v_and_or_b32 v8, v8, s75, v14
	v_bitop3_b32 v172, v3, v5, v7 bitop3:0xde
	v_or_b32_e32 v3, 64, v148
	v_mul_i32_i24_e32 v15, -4, v169
	v_add3_u32 v169, v12, 0, v8
	v_and_b32_e32 v12, 0xc0, v13
	v_and_b32_e32 v13, 48, v9
	v_bitop3_b32 v173, v3, v5, v7 bitop3:0xde
	v_or_b32_e32 v3, 0x60, v148
	v_or3_b32 v8, v11, v12, v13
	v_mov_b32_e32 v9, v149
	v_bitop3_b32 v171, v148, v5, v7 bitop3:0xde
	v_bitop3_b32 v174, v3, v5, v7 bitop3:0xde
	v_mov_b32_e32 v3, v149
	v_mov_b32_e32 v5, v149
	v_mov_b32_e32 v7, v149
	v_lshl_add_u64 v[150:151], s[48:49], 0, v[8:9]
	v_mov_b32_e32 v240, v8
	v_or3_b32 v8, v10, v12, v13
	v_mov_b32_e32 v16, v149
	v_mov_b32_e32 v17, v149
	v_and_b32_e32 v170, 63, v168
	s_lshl_b32 s46, s80, 2
	v_lshl_add_u32 v168, v167, 2, s65
	v_lshl_add_u64 v[152:153], s[48:49], 0, v[8:9]
	v_mov_b32_e32 v241, v8
	v_lshl_add_u64 v[154:155], s[50:51], 0, v[6:7]
	v_mov_b32_e32 v242, v6
	v_lshl_add_u64 v[156:157], s[50:51], 0, v[4:5]
	v_mov_b32_e32 v243, v4
	v_lshl_add_u64 v[158:159], s[50:51], 0, v[2:3]
	v_mov_b32_e32 v244, v2
	s_add_u32 s94, s2, s50
	s_addc_u32 s95, s3, s51
	s_add_u32 s96, s2, s48
	s_addc_u32 s97, s3, s49
	v_add3_u32 v167, s63, v15, v167
	v_mov_b32_e32 v2, v149
	v_mov_b32_e32 v4, v149
	v_mov_b32_e32 v6, v149
	v_mov_b32_e32 v8, v149
	v_mov_b32_e32 v10, v149
	v_mov_b32_e32 v11, v149
	v_mov_b32_e32 v12, v149
	v_mov_b32_e32 v13, v149
	v_mov_b32_e32 v14, v149
	v_mov_b32_e32 v15, v149
	v_mov_b64_e32 v[32:33], v[16:17]
	v_mov_b64_e32 v[48:49], v[16:17]
	v_mov_b64_e32 v[64:65], v[16:17]
	s_add_i32 s46, s46, 4
	v_cmp_gt_u32_e64 s[0:1], 32, v170
	v_mov_b32_e32 v176, 0
	v_mov_b32_e32 v175, 0
	v_mov_b32_e32 v210, 0
	v_mov_b32_e32 v211, 0
	v_mov_b32_e32 v212, 0
	v_mov_b32_e32 v213, 0
	v_mov_b32_e32 v214, 0
	v_mov_b32_e32 v215, 0
	v_mov_b32_e32 v216, 0
	v_mov_b32_e32 v217, 0
	v_mov_b32_e32 v218, 0
	v_mov_b32_e32 v219, 0
	v_mov_b32_e32 v220, 0
	v_mov_b32_e32 v221, 0
	v_mov_b32_e32 v222, 0
	v_mov_b32_e32 v223, 0
	v_mov_b32_e32 v224, 0
	v_mov_b32_e32 v225, 0
	s_movk_i32 s47, 0xff00
	v_mov_b64_e32 v[30:31], v[14:15]
	v_mov_b64_e32 v[28:29], v[12:13]
	v_mov_b64_e32 v[26:27], v[10:11]
	v_mov_b64_e32 v[24:25], v[8:9]
	v_mov_b64_e32 v[22:23], v[6:7]
	v_mov_b64_e32 v[20:21], v[4:5]
	v_mov_b64_e32 v[18:19], v[2:3]
	v_mov_b64_e32 v[46:47], v[14:15]
	v_mov_b64_e32 v[44:45], v[12:13]
	v_mov_b64_e32 v[42:43], v[10:11]
	v_mov_b64_e32 v[40:41], v[8:9]
	v_mov_b64_e32 v[38:39], v[6:7]
	v_mov_b64_e32 v[36:37], v[4:5]
	v_mov_b64_e32 v[34:35], v[2:3]
	v_mov_b64_e32 v[62:63], v[14:15]
	v_mov_b64_e32 v[60:61], v[12:13]
	v_mov_b64_e32 v[58:59], v[10:11]
	v_mov_b64_e32 v[56:57], v[8:9]
	v_mov_b64_e32 v[54:55], v[6:7]
	v_mov_b64_e32 v[52:53], v[4:5]
	v_mov_b64_e32 v[50:51], v[2:3]
.LBB0_946:
	s_add_i32 s44, s12, -1
	s_waitcnt vmcnt(0)
	s_and_b32 s48, s44, 1
	s_cmp_ge_u32 s12, s46
	s_waitcnt vmcnt(0) lgkmcnt(0)
	s_barrier
	s_cbranch_scc1 .LBB0_948
	s_xor_b32 s44, s48, 1
	s_mulk_i32 s44, 0x6000
	s_add_i32 s44, s64, s44
	s_add_i32 m0, s44, 0x8000
	s_nop 0
	global_load_lds_dwordx4 v244, s[94:95]
	s_add_i32 m0, s44, 0xa000
	s_nop 0
	global_load_lds_dwordx4 v243, s[94:95]
	s_add_i32 m0, s44, 0xc000
	s_lshl_b32 s44, s48, 14
	s_xor_b32 s44, s44, 0x4000
	s_add_i32 s44, s64, s44
	global_load_lds_dwordx4 v242, s[94:95]
	s_mov_b32 m0, s44
	s_nop 0
	global_load_lds_dwordx4 v241, s[96:97]
	s_add_i32 m0, s44, 0x2000
	s_nop 0
	global_load_lds_dwordx4 v240, s[96:97]



.LBB0_954:
	v_add_f32_e32 v81, v81, v97
	v_fmac_f32_e32 v81, v176, v96
	v_cvt_pk_bf16_f32 v176, v177, v178
	v_cvt_pk_bf16_f32 v177, v83, v84
	v_cvt_pk_bf16_f32 v178, v85, v86
	v_cvt_pk_bf16_f32 v179, v87, v179
	v_cvt_pk_bf16_f32 v84, v88, v89
	v_cvt_pk_bf16_f32 v85, v90, v91
	v_cvt_pk_bf16_f32 v86, v92, v93
	v_cvt_pk_bf16_f32 v87, v94, v95
	v_cvt_pk_bf16_f32 v66, v66, v67
	v_cvt_pk_bf16_f32 v67, v68, v69
	v_cvt_pk_bf16_f32 v68, v70, v71
	v_cvt_pk_bf16_f32 v69, v72, v82
	v_cvt_pk_bf16_f32 v70, v73, v74
	v_cvt_pk_bf16_f32 v71, v75, v76
	v_cvt_pk_bf16_f32 v72, v77, v78
	v_cvt_pk_bf16_f32 v73, v79, v80
	v_lshl_add_u32 v78, s48, 14, v169
	ds_read_b64_tr_b16 v[74:75], v78 offset:0
	ds_read_b64_tr_b16 v[76:77], v78 offset:0x800
	ds_read_b64_tr_b16 v[88:89], v78 offset:0x1000
	ds_read_b64_tr_b16 v[90:91], v78 offset:0x1800
	ds_read_b64_tr_b16 v[92:93], v78 offset:0x2000
	ds_read_b64_tr_b16 v[94:95], v78 offset:0x2800
	ds_read_b64_tr_b16 v[180:181], v78 offset:0x3000
	ds_read_b64_tr_b16 v[182:183], v78 offset:0x3800
	ds_read_b64_tr_b16 v[184:185], v78 offset:0x200
	ds_read_b64_tr_b16 v[186:187], v78 offset:0xa00
	ds_read_b64_tr_b16 v[188:189], v78 offset:0x1200
	ds_read_b64_tr_b16 v[190:191], v78 offset:0x1a00
	ds_read_b64_tr_b16 v[192:193], v78 offset:0x2200
	ds_read_b64_tr_b16 v[194:195], v78 offset:0x2a00
	ds_read_b64_tr_b16 v[196:197], v78 offset:0x3200
	ds_read_b64_tr_b16 v[198:199], v78 offset:0x3a00
	s_waitcnt lgkmcnt(8)
	v_permlane32_swap_b32_e32 v176, v178
	v_permlane32_swap_b32_e32 v177, v179
	v_permlane32_swap_b32_e32 v84, v86
	v_permlane32_swap_b32_e32 v85, v87
	v_permlane32_swap_b32_e32 v66, v68
	v_permlane32_swap_b32_e32 v67, v69
	v_permlane32_swap_b32_e32 v70, v72
	v_permlane32_swap_b32_e32 v71, v73
	v_mfma_f32_32x32x16_bf16 v[50:65], v[176:179], v[74:77], v[50:65]
	ds_read_b64_tr_b16 v[74:75], v78 offset:0x400
	ds_read_b64_tr_b16 v[76:77], v78 offset:0xc00
	v_mfma_f32_32x32x16_bf16 v[50:65], v[84:87], v[88:91], v[50:65]
	ds_read_b64_tr_b16 v[88:89], v78 offset:0x1400
	ds_read_b64_tr_b16 v[90:91], v78 offset:0x1c00
	v_mfma_f32_32x32x16_bf16 v[50:65], v[66:69], v[92:95], v[50:65]
	ds_read_b64_tr_b16 v[92:93], v78 offset:0x2400
	ds_read_b64_tr_b16 v[94:95], v78 offset:0x2c00
	ds_read_b64_tr_b16 v[200:201], v78 offset:0x3400
	ds_read_b64_tr_b16 v[202:203], v78 offset:0x3c00
	s_waitcnt lgkmcnt(8)
	v_mfma_f32_32x32x16_bf16 v[50:65], v[70:73], v[180:183], v[50:65]
	v_mfma_f32_32x32x16_bf16 v[34:49], v[176:179], v[184:187], v[34:49]
	ds_read_b64_tr_b16 v[180:181], v78 offset:0x600
	ds_read_b64_tr_b16 v[182:183], v78 offset:0xe00
	ds_read_b64_tr_b16 v[184:185], v78 offset:0x1600
	ds_read_b64_tr_b16 v[186:187], v78 offset:0x1e00
	v_mfma_f32_32x32x16_bf16 v[34:49], v[84:87], v[188:191], v[34:49]
	ds_read_b64_tr_b16 v[188:189], v78 offset:0x2600
	ds_read_b64_tr_b16 v[190:191], v78 offset:0x2e00
	v_mfma_f32_32x32x16_bf16 v[34:49], v[66:69], v[192:195], v[34:49]
	ds_read_b64_tr_b16 v[192:193], v78 offset:0x3600
	ds_read_b64_tr_b16 v[194:195], v78 offset:0x3e00
	s_waitcnt lgkmcnt(8)
	v_mfma_f32_32x32x16_bf16 v[34:49], v[70:73], v[196:199], v[34:49]
	v_mfma_f32_32x32x16_bf16 v[18:33], v[176:179], v[74:77], v[18:33]
	s_waitcnt lgkmcnt(0)
	v_mfma_f32_32x32x16_bf16 v[18:33], v[84:87], v[88:91], v[18:33]
	v_mfma_f32_32x32x16_bf16 v[18:33], v[66:69], v[92:95], v[18:33]
	v_mfma_f32_32x32x16_bf16 v[18:33], v[70:73], v[200:203], v[18:33]
	v_mfma_f32_32x32x16_bf16 v[2:17], v[176:179], v[180:183], v[2:17]
	s_add_i32 s47, s47, 64
	s_add_i32 s12, s12, 1
	s_add_u32 s94, s94, s16
	s_addc_u32 s95, s95, s17
	s_add_u32 s96, s96, s14
	s_addc_u32 s97, s97, s15


	v_mfma_f32_32x32x16_bf16 v[2:17], v[84:87], v[184:187], v[2:17]
	v_subrev_u32_e32 v167, 64, v167
	s_cmp_eq_u32 s54, s47
	v_mfma_f32_32x32x16_bf16 v[2:17], v[66:69], v[188:191], v[2:17]
	v_mfma_f32_32x32x16_bf16 v[2:17], v[70:73], v[192:195], v[2:17]
	s_cbranch_scc1 .LBB0_956
	v_mov_b32_e32 v176, v81
	s_add_i32 s44, s47, 0xe0
	s_cmp_ge_i32 s44, s55
	s_cbranch_scc0 .LBB0_946

.Latt2_drain_nodma:
	s_add_i32 s47, s47, 64
	s_add_i32 s12, s12, 1
	s_add_u32 s94, s94, s16
	s_addc_u32 s95, s95, s17
	s_add_u32 s96, s96, s14
	s_addc_u32 s97, s97, s15
	s_cmp_eq_u32 s54, s47
	s_cbranch_scc0 .Latt2_drain
	s_branch .LBB0_956
